# v092 + grid seam after the conv|F|carry phase replaced by a carry-done counter hand-off (carry bytes stored write-through)
# baseline (speedup 1.0000x reference)
; #define GAS __attribute__((address_space(1)))
; __device__ __forceinline__ void phase_carry(Frame& F, int l) {
;     const int gt = F.vcu * 512 + F.tid; if (gt >= NB * NG * 2 * SP) return;
;     const int p = gt & 63, d = (gt >> 6) & 1, g = (gt >> 7) & 31, b = gt >> 12;
;     const f32x2 lt = WSP(f32x2, WS_LT)[((l * NG + g) * 2 + d) * 64 + p];
;     const float* Fb = WSP(float, WS_F); unsigned char* a8 = WSP(unsigned char, WS_A8);
;     float hr = 0.f, hi = 0.f;
;     float frv[36], fiv[36];
; #pragma unroll
;     for (int step = 0; step < 36; ++step) {
;         int inst; if (step < 4) inst = 256 + b * 4 + (d == 0 ? step : 3 - step); else inst = b * 32 + (d == 0 ? step - 4 : 35 - step);
;         const size_t row = (size_t)g * NINST + inst;
;         frv[step] = *(const GAS float*)(Fb + row * 256 + d * 128 + p); fiv[step] = *(const GAS float*)(Fb + row * 256 + d * 128 + 64 + p); }
.Lfd0_479:
	s_nop 0
	v_lshl_add_u32 v1, s0, 9, v0
	s_mov_b32 s0, 0x8000
	v_cmp_gt_i32_e32 vcc, s0, v1
	s_and_saveexec_b64 s[4:5], vcc
	s_cbranch_execz .Lfd0_481
	v_bfe_u32 v17, v0, 6, 1
	v_bfe_u32 v7, v1, 7, 5
	v_and_b32_e32 v6, 63, v0
	v_ashrrev_i32_e32 v10, 12, v1
	v_lshlrev_b32_e32 v1, 7, v7
	v_lshlrev_b32_e32 v2, 6, v17
	v_or3_b32 v1, v1, v2, v6
	v_lshlrev_b32_e32 v2, 3, v1
	v_mov_b32_e32 v3, 0
	v_lshl_add_u64 v[4:5], s[2:3], 0, v[2:3]
	v_add_co_u32_e32 v4, vcc, 0x280000, v4
	v_lshlrev_b32_e32 v12, 2, v10
	s_nop 0
	v_addc_co_u32_e32 v5, vcc, 0, v5, vcc
	v_lshlrev_b32_e32 v8, 9, v17
	v_mov_b32_e32 v9, v3
	v_add_u32_e32 v14, 0x100, v12
	v_cmp_eq_u32_e32 vcc, 0, v17
	v_bfe_i32 v16, v0, 6, 1
	flat_load_dwordx2 v[4:5], v[4:5]
	v_lshl_add_u64 v[8:9], s[2:3], 0, v[8:9]
	s_mov_b64 s[0:1], 0x56900000
	v_lshlrev_b32_e32 v1, 5, v10
	v_or_b32_e32 v10, v17, v14
	v_sub_u32_e32 v12, v12, v17
	v_cndmask_b32_e64 v15, 0, 3, vcc
	v_lshl_add_u64 v[80:81], v[8:9], 0, s[0:1]
	v_and_or_b32 v8, v16, 3, v14
	v_add_u32_e32 v10, 1, v10
	v_add_u32_e32 v12, 0x102, v12
	v_or_b32_e32 v14, v14, v15
	v_lshlrev_b32_e32 v2, 9, v7
	v_ashrrev_i32_e32 v9, 31, v8
	v_ashrrev_i32_e32 v11, 31, v10
	v_ashrrev_i32_e32 v13, 31, v12
	v_ashrrev_i32_e32 v15, 31, v14
	v_lshl_add_u64 v[78:79], v[8:9], 0, v[2:3]
	v_lshl_add_u64 v[74:75], v[10:11], 0, v[2:3]
	v_lshl_add_u64 v[72:73], v[12:13], 0, v[2:3]
	v_lshl_add_u64 v[70:71], v[14:15], 0, v[2:3]
	v_lshlrev_b64 v[8:9], 10, v[78:79]
	v_lshlrev_b64 v[10:11], 10, v[74:75]
	v_lshlrev_b64 v[12:13], 10, v[72:73]
	v_lshlrev_b64 v[14:15], 10, v[70:71]
	v_lshl_add_u64 v[8:9], v[80:81], 0, v[8:9]
	v_lshlrev_b32_e32 v82, 2, v6
	v_mov_b32_e32 v83, v3
	v_lshl_add_u64 v[10:11], v[80:81], 0, v[10:11]
	v_lshl_add_u64 v[12:13], v[80:81], 0, v[12:13]
	v_lshl_add_u64 v[14:15], v[80:81], 0, v[14:15]
	v_lshl_add_u64 v[8:9], v[8:9], 0, v[82:83]
	v_lshl_add_u64 v[10:11], v[10:11], 0, v[82:83]
	v_lshl_add_u64 v[12:13], v[12:13], 0, v[82:83]
	v_lshl_add_u64 v[14:15], v[14:15], 0, v[82:83]
	global_load_dword v115, v[8:9], off
	global_load_dword v122, v[8:9], off offset:256
	global_load_dword v123, v[10:11], off
	global_load_dword v124, v[10:11], off offset:256
	global_load_dword v125, v[12:13], off
	global_load_dword v113, v[12:13], off offset:256
	global_load_dword v111, v[14:15], off
	global_load_dword v109, v[14:15], off offset:256
	v_and_or_b32 v8, v16, 31, v1
	v_cndmask_b32_e64 v10, 30, 1, vcc
	v_cndmask_b32_e64 v12, 29, 2, vcc
	v_cndmask_b32_e64 v14, 28, 3, vcc
	v_ashrrev_i32_e32 v9, 31, v8
	v_or_b32_e32 v10, v1, v10
	v_or_b32_e32 v12, v1, v12
	v_or_b32_e32 v14, v1, v14
	v_lshl_add_u64 v[68:69], v[8:9], 0, v[2:3]
	v_ashrrev_i32_e32 v11, 31, v10
	v_ashrrev_i32_e32 v13, 31, v12
	v_ashrrev_i32_e32 v15, 31, v14
	v_lshlrev_b64 v[8:9], 10, v[68:69]
	v_lshl_add_u64 v[66:67], v[10:11], 0, v[2:3]
	v_lshl_add_u64 v[64:65], v[12:13], 0, v[2:3]
	v_lshl_add_u64 v[62:63], v[14:15], 0, v[2:3]
	v_lshl_add_u64 v[8:9], v[80:81], 0, v[8:9]
	v_lshlrev_b64 v[10:11], 10, v[66:67]
	v_lshlrev_b64 v[12:13], 10, v[64:65]
	v_lshlrev_b64 v[14:15], 10, v[62:63]
	v_lshl_add_u64 v[8:9], v[8:9], 0, v[82:83]
	v_lshl_add_u64 v[10:11], v[80:81], 0, v[10:11]
	v_lshl_add_u64 v[12:13], v[80:81], 0, v[12:13]
	v_lshl_add_u64 v[14:15], v[80:81], 0, v[14:15]
	v_lshl_add_u64 v[10:11], v[10:11], 0, v[82:83]
	v_lshl_add_u64 v[12:13], v[12:13], 0, v[82:83]
	v_lshl_add_u64 v[14:15], v[14:15], 0, v[82:83]
	global_load_dword v114, v[8:9], off
	global_load_dword v112, v[8:9], off offset:256
	global_load_dword v110, v[10:11], off
	global_load_dword v108, v[10:11], off offset:256
	global_load_dword v107, v[12:13], off
	global_load_dword v105, v[12:13], off offset:256
	global_load_dword v103, v[14:15], off
	global_load_dword v101, v[14:15], off offset:256
	v_cndmask_b32_e64 v8, 27, 4, vcc
	v_or_b32_e32 v8, v1, v8
	v_cndmask_b32_e64 v10, 26, 5, vcc
	v_cndmask_b32_e64 v12, 25, 6, vcc
	v_cndmask_b32_e64 v14, 24, 7, vcc
	v_ashrrev_i32_e32 v9, 31, v8
	v_or_b32_e32 v10, v1, v10
	v_or_b32_e32 v12, v1, v12
	v_or_b32_e32 v14, v1, v14
	v_lshl_add_u64 v[60:61], v[8:9], 0, v[2:3]
	v_ashrrev_i32_e32 v11, 31, v10
	v_ashrrev_i32_e32 v13, 31, v12
	v_ashrrev_i32_e32 v15, 31, v14
	v_lshlrev_b64 v[8:9], 10, v[60:61]
	v_lshl_add_u64 v[58:59], v[10:11], 0, v[2:3]
	v_lshl_add_u64 v[56:57], v[12:13], 0, v[2:3]
	v_lshl_add_u64 v[54:55], v[14:15], 0, v[2:3]
	v_lshl_add_u64 v[8:9], v[80:81], 0, v[8:9]
	v_lshlrev_b64 v[10:11], 10, v[58:59]
	v_lshlrev_b64 v[12:13], 10, v[56:57]
	v_lshlrev_b64 v[14:15], 10, v[54:55]
	v_lshl_add_u64 v[8:9], v[8:9], 0, v[82:83]
	v_lshl_add_u64 v[10:11], v[80:81], 0, v[10:11]
	v_lshl_add_u64 v[12:13], v[80:81], 0, v[12:13]
	v_lshl_add_u64 v[14:15], v[80:81], 0, v[14:15]
	v_lshl_add_u64 v[10:11], v[10:11], 0, v[82:83]
	v_lshl_add_u64 v[12:13], v[12:13], 0, v[82:83]
	v_lshl_add_u64 v[14:15], v[14:15], 0, v[82:83]
	global_load_dword v106, v[8:9], off
	global_load_dword v104, v[8:9], off offset:256
	global_load_dword v102, v[10:11], off
	global_load_dword v100, v[10:11], off offset:256
	global_load_dword v99, v[12:13], off
	global_load_dword v97, v[12:13], off offset:256
	global_load_dword v95, v[14:15], off
	global_load_dword v93, v[14:15], off offset:256
	v_cndmask_b32_e64 v8, 23, 8, vcc
	v_or_b32_e32 v8, v1, v8
	v_cndmask_b32_e64 v10, 22, 9, vcc
	v_cndmask_b32_e64 v12, 21, 10, vcc
	v_cndmask_b32_e64 v14, 20, 11, vcc
	v_ashrrev_i32_e32 v9, 31, v8
	v_or_b32_e32 v10, v1, v10
	v_or_b32_e32 v12, v1, v12
	v_or_b32_e32 v14, v1, v14
	v_lshl_add_u64 v[52:53], v[8:9], 0, v[2:3]
	v_ashrrev_i32_e32 v11, 31, v10
	v_ashrrev_i32_e32 v13, 31, v12
	v_ashrrev_i32_e32 v15, 31, v14
	v_lshlrev_b64 v[8:9], 10, v[52:53]
; #define GAS __attribute__((address_space(1)))
; __device__ __forceinline__ void phase_carry(Frame& F, int l) {
;     ...
; #pragma unroll
;     for (int step = 0; step < 36; ++step) {
;         int inst; if (step < 4) inst = 256 + b * 4 + (d == 0 ? step : 3 - step); else inst = b * 32 + (d == 0 ? step - 4 : 35 - step);
;         const size_t row = (size_t)g * NINST + inst;
;         frv[step] = *(const GAS float*)(Fb + row * 256 + d * 128 + p); fiv[step] = *(const GAS float*)(Fb + row * 256 + d * 128 + 64 + p); }
	v_lshl_add_u64 v[50:51], v[10:11], 0, v[2:3]
	v_lshl_add_u64 v[48:49], v[12:13], 0, v[2:3]
	v_lshl_add_u64 v[46:47], v[14:15], 0, v[2:3]
	v_lshl_add_u64 v[8:9], v[80:81], 0, v[8:9]
	v_lshlrev_b64 v[10:11], 10, v[50:51]
	v_lshlrev_b64 v[12:13], 10, v[48:49]
	v_lshlrev_b64 v[14:15], 10, v[46:47]
	v_lshl_add_u64 v[8:9], v[8:9], 0, v[82:83]
	v_lshl_add_u64 v[10:11], v[80:81], 0, v[10:11]
	v_lshl_add_u64 v[12:13], v[80:81], 0, v[12:13]
	v_lshl_add_u64 v[14:15], v[80:81], 0, v[14:15]
	v_lshl_add_u64 v[10:11], v[10:11], 0, v[82:83]
	v_lshl_add_u64 v[12:13], v[12:13], 0, v[82:83]
	v_lshl_add_u64 v[14:15], v[14:15], 0, v[82:83]
	global_load_dword v98, v[8:9], off
	global_load_dword v96, v[8:9], off offset:256
	global_load_dword v94, v[10:11], off
	global_load_dword v92, v[10:11], off offset:256
	global_load_dword v91, v[12:13], off
	global_load_dword v89, v[12:13], off offset:256
	global_load_dword v87, v[14:15], off
	global_load_dword v85, v[14:15], off offset:256
	v_cndmask_b32_e64 v8, 19, 12, vcc
	v_or_b32_e32 v8, v1, v8
	v_cndmask_b32_e64 v10, 18, 13, vcc
	v_cndmask_b32_e64 v12, 17, 14, vcc
	v_or_b32_e32 v14, v17, v1
	v_ashrrev_i32_e32 v9, 31, v8
	v_or_b32_e32 v10, v1, v10
	v_or_b32_e32 v12, v1, v12
	v_add_u32_e32 v14, 15, v14
	v_lshl_add_u64 v[44:45], v[8:9], 0, v[2:3]
	v_ashrrev_i32_e32 v11, 31, v10
	v_ashrrev_i32_e32 v13, 31, v12
	v_ashrrev_i32_e32 v15, 31, v14
	v_lshlrev_b64 v[8:9], 10, v[44:45]
	v_lshl_add_u64 v[42:43], v[10:11], 0, v[2:3]
	v_lshl_add_u64 v[40:41], v[12:13], 0, v[2:3]
	v_lshl_add_u64 v[38:39], v[14:15], 0, v[2:3]
	v_lshl_add_u64 v[8:9], v[80:81], 0, v[8:9]
	v_lshlrev_b64 v[10:11], 10, v[42:43]
	v_lshlrev_b64 v[12:13], 10, v[40:41]
	v_lshlrev_b64 v[14:15], 10, v[38:39]
	v_lshl_add_u64 v[8:9], v[8:9], 0, v[82:83]
	v_lshl_add_u64 v[10:11], v[80:81], 0, v[10:11]
	v_lshl_add_u64 v[12:13], v[80:81], 0, v[12:13]
	v_lshl_add_u64 v[14:15], v[80:81], 0, v[14:15]
	v_lshl_add_u64 v[10:11], v[10:11], 0, v[82:83]
	v_lshl_add_u64 v[12:13], v[12:13], 0, v[82:83]
	v_lshl_add_u64 v[14:15], v[14:15], 0, v[82:83]
	global_load_dword v90, v[8:9], off
	global_load_dword v88, v[8:9], off offset:256
	global_load_dword v86, v[10:11], off
	global_load_dword v84, v[10:11], off offset:256
	global_load_dword v79, v[12:13], off
	global_load_dword v73, v[12:13], off offset:256
	global_load_dword v69, v[14:15], off
	global_load_dword v65, v[14:15], off offset:256
	v_sub_u32_e32 v8, v1, v17
	v_add_u32_e32 v8, 16, v8
	v_cndmask_b32_e64 v10, 14, 17, vcc
	v_cndmask_b32_e64 v12, 13, 18, vcc
	v_cndmask_b32_e64 v14, 12, 19, vcc
	v_ashrrev_i32_e32 v9, 31, v8
	v_or_b32_e32 v10, v1, v10
	v_or_b32_e32 v12, v1, v12
	v_or_b32_e32 v14, v1, v14
	v_lshl_add_u64 v[36:37], v[8:9], 0, v[2:3]
	v_ashrrev_i32_e32 v11, 31, v10
	v_ashrrev_i32_e32 v13, 31, v12
	v_ashrrev_i32_e32 v15, 31, v14
	v_lshlrev_b64 v[8:9], 10, v[36:37]
	v_lshl_add_u64 v[34:35], v[10:11], 0, v[2:3]
	v_lshl_add_u64 v[32:33], v[12:13], 0, v[2:3]
	v_lshl_add_u64 v[30:31], v[14:15], 0, v[2:3]
	v_lshl_add_u64 v[8:9], v[80:81], 0, v[8:9]
	v_lshlrev_b64 v[10:11], 10, v[34:35]
	v_lshlrev_b64 v[12:13], 10, v[32:33]
	v_lshlrev_b64 v[14:15], 10, v[30:31]
	v_lshl_add_u64 v[8:9], v[8:9], 0, v[82:83]
	v_lshl_add_u64 v[10:11], v[80:81], 0, v[10:11]
	v_lshl_add_u64 v[12:13], v[80:81], 0, v[12:13]
	v_lshl_add_u64 v[14:15], v[80:81], 0, v[14:15]
	v_lshl_add_u64 v[10:11], v[10:11], 0, v[82:83]
	v_lshl_add_u64 v[12:13], v[12:13], 0, v[82:83]
	v_lshl_add_u64 v[14:15], v[14:15], 0, v[82:83]
	global_load_dword v75, v[8:9], off
	global_load_dword v71, v[8:9], off offset:256
	global_load_dword v67, v[10:11], off
	global_load_dword v63, v[10:11], off offset:256
	global_load_dword v61, v[12:13], off
	global_load_dword v57, v[12:13], off offset:256
	global_load_dword v53, v[14:15], off
	global_load_dword v49, v[14:15], off offset:256
	v_cndmask_b32_e64 v8, 11, 20, vcc
	v_or_b32_e32 v8, v1, v8
	v_cndmask_b32_e64 v10, 10, 21, vcc
	v_cndmask_b32_e64 v12, 9, 22, vcc
	v_cndmask_b32_e64 v14, 8, 23, vcc
	v_ashrrev_i32_e32 v9, 31, v8
	v_or_b32_e32 v10, v1, v10
	v_or_b32_e32 v12, v1, v12
	v_or_b32_e32 v14, v1, v14
	v_lshl_add_u64 v[28:29], v[8:9], 0, v[2:3]
	v_ashrrev_i32_e32 v11, 31, v10
	v_ashrrev_i32_e32 v13, 31, v12
	v_ashrrev_i32_e32 v15, 31, v14
	v_lshlrev_b64 v[8:9], 10, v[28:29]
	v_lshl_add_u64 v[26:27], v[10:11], 0, v[2:3]
	v_lshl_add_u64 v[24:25], v[12:13], 0, v[2:3]
	v_lshl_add_u64 v[22:23], v[14:15], 0, v[2:3]
	v_lshl_add_u64 v[8:9], v[80:81], 0, v[8:9]
	v_lshlrev_b64 v[10:11], 10, v[26:27]
	v_lshlrev_b64 v[12:13], 10, v[24:25]
	v_lshlrev_b64 v[14:15], 10, v[22:23]
	v_lshl_add_u64 v[8:9], v[8:9], 0, v[82:83]
	v_lshl_add_u64 v[10:11], v[80:81], 0, v[10:11]
	v_lshl_add_u64 v[12:13], v[80:81], 0, v[12:13]
	v_lshl_add_u64 v[14:15], v[80:81], 0, v[14:15]
	v_lshl_add_u64 v[10:11], v[10:11], 0, v[82:83]
	v_lshl_add_u64 v[12:13], v[12:13], 0, v[82:83]
	v_lshl_add_u64 v[14:15], v[14:15], 0, v[82:83]
	global_load_dword v59, v[8:9], off
	global_load_dword v55, v[8:9], off offset:256
	global_load_dword v51, v[10:11], off
	global_load_dword v47, v[10:11], off offset:256
	global_load_dword v45, v[12:13], off
	global_load_dword v41, v[12:13], off offset:256
	global_load_dword v37, v[14:15], off
	global_load_dword v33, v[14:15], off offset:256
	v_cndmask_b32_e64 v8, 7, 24, vcc
	v_or_b32_e32 v8, v1, v8
	v_cndmask_b32_e64 v10, 6, 25, vcc
	v_cndmask_b32_e64 v12, 5, 26, vcc
	v_cndmask_b32_e64 v14, 4, 27, vcc
	v_ashrrev_i32_e32 v9, 31, v8
	v_or_b32_e32 v10, v1, v10
	v_or_b32_e32 v12, v1, v12
	v_or_b32_e32 v14, v1, v14
	v_lshl_add_u64 v[20:21], v[8:9], 0, v[2:3]
	v_ashrrev_i32_e32 v11, 31, v10
	v_ashrrev_i32_e32 v13, 31, v12
	v_ashrrev_i32_e32 v15, 31, v14
; #define GAS __attribute__((address_space(1)))
; __device__ __forceinline__ void phase_carry(Frame& F, int l) {
;     ...
; #pragma unroll
;     for (int step = 0; step < 36; ++step) {
;         int inst; if (step < 4) inst = 256 + b * 4 + (d == 0 ? step : 3 - step); else inst = b * 32 + (d == 0 ? step - 4 : 35 - step);
;         const size_t row = (size_t)g * NINST + inst;
;         frv[step] = *(const GAS float*)(Fb + row * 256 + d * 128 + p); fiv[step] = *(const GAS float*)(Fb + row * 256 + d * 128 + 64 + p); }
; #pragma unroll
;     for (int step = 0; step < 36; ++step) {
;         int inst; if (step < 4) inst = 256 + b * 4 + (d == 0 ? step : 3 - step); else inst = b * 32 + (d == 0 ? step - 4 : 35 - step);
;         const size_t row = (size_t)g * NINST + inst;
;         a8[row * KS2 + 1024 + d * 128 + p] = (unsigned char)(pk4_fp8(hr * S5_SH, 0.f, 0.f, 0.f) & 0xffu); a8[row * KS2 + 1024 + d * 128 + 64 + p] = (unsigned char)(pk4_fp8(hi * S5_SH, 0.f, 0.f, 0.f) & 0xffu);
;         const float nr = lt.x * hr - lt.y * hi + frv[step]; hi = lt.x * hi + lt.y * hr + fiv[step]; hr = nr; }
	v_lshlrev_b32_e32 v76, 7, v17
	v_lshlrev_b64 v[8:9], 10, v[20:21]
	v_lshl_add_u64 v[18:19], v[10:11], 0, v[2:3]
	v_lshl_add_u64 v[16:17], v[12:13], 0, v[2:3]
	v_lshl_add_u64 v[14:15], v[14:15], 0, v[2:3]
	v_lshl_add_u64 v[8:9], v[80:81], 0, v[8:9]
	v_lshlrev_b64 v[10:11], 10, v[18:19]
	v_lshlrev_b64 v[12:13], 10, v[16:17]
	v_lshlrev_b64 v[116:117], 10, v[14:15]
	v_lshl_add_u64 v[8:9], v[8:9], 0, v[82:83]
	v_lshl_add_u64 v[10:11], v[80:81], 0, v[10:11]
	v_lshl_add_u64 v[12:13], v[80:81], 0, v[12:13]
	v_lshl_add_u64 v[116:117], v[80:81], 0, v[116:117]
	v_lshl_add_u64 v[10:11], v[10:11], 0, v[82:83]
	v_lshl_add_u64 v[12:13], v[12:13], 0, v[82:83]
	v_lshl_add_u64 v[116:117], v[116:117], 0, v[82:83]
	global_load_dword v43, v[8:9], off
	global_load_dword v39, v[8:9], off offset:256
	global_load_dword v35, v[10:11], off
	global_load_dword v31, v[10:11], off offset:256
	global_load_dword v29, v[12:13], off
	global_load_dword v27, v[12:13], off offset:256
	global_load_dword v21, v[116:117], off
	global_load_dword v19, v[116:117], off offset:256
	v_cndmask_b32_e64 v8, 3, 28, vcc
	v_or_b32_e32 v8, v1, v8
	v_ashrrev_i32_e32 v9, 31, v8
	v_lshl_add_u64 v[12:13], v[8:9], 0, v[2:3]
	v_lshlrev_b64 v[8:9], 10, v[12:13]
	v_lshl_add_u64 v[8:9], v[80:81], 0, v[8:9]
	v_lshl_add_u64 v[116:117], v[8:9], 0, v[82:83]
	v_cndmask_b32_e64 v8, 2, 29, vcc
	v_or_b32_e32 v8, v1, v8
	v_ashrrev_i32_e32 v9, 31, v8
	v_lshl_add_u64 v[10:11], v[8:9], 0, v[2:3]
	v_lshlrev_b64 v[8:9], 10, v[10:11]
	v_lshl_add_u64 v[8:9], v[80:81], 0, v[8:9]
	v_lshl_add_u64 v[118:119], v[8:9], 0, v[82:83]
	v_cndmask_b32_e64 v8, 1, 30, vcc
	v_or_b32_e32 v8, v1, v8
	v_ashrrev_i32_e32 v9, 31, v8
	v_lshl_add_u64 v[8:9], v[8:9], 0, v[2:3]
	v_lshlrev_b64 v[120:121], 10, v[8:9]
	v_lshl_add_u64 v[80:81], v[80:81], 0, v[120:121]
	v_lshl_add_u64 v[80:81], v[80:81], 0, v[82:83]
	global_load_dword v25, v[116:117], off
	global_load_dword v23, v[116:117], off offset:256
	global_load_dword v17, v[118:119], off
	global_load_dword v15, v[118:119], off offset:256
	global_load_dword v11, v[80:81], off
	global_load_dword v9, v[80:81], off offset:256
	v_mov_b32_e32 v80, v3
	v_cvt_pk_fp8_f32 v80, 0, 0
	v_mov_b32_e32 v77, v3
	v_mov_b32_e32 v7, v3
	v_lshl_add_u64 v[76:77], s[2:3], 0, v[76:77]
	v_cvt_pk_fp8_f32 v80, 0, 0 op_sel:[0,0,1]
	v_lshl_add_u64 v[6:7], v[76:77], 0, v[6:7]
	s_mov_b64 s[0:1], 0x6ab00400
	v_mul_hi_i32_i24_e32 v77, 0x500, v78
	v_mul_i32_i24_e32 v76, 0x500, v78
	s_waitcnt vmcnt(0) lgkmcnt(0)
	v_mul_f32_e32 v78, 0, v5
	v_lshl_add_u64 v[6:7], v[6:7], 0, s[0:1]
	v_fma_f32 v13, v4, 0, -v78
	v_fmac_f32_e32 v78, 0, v4
	v_lshl_add_u64 v[76:77], v[6:7], 0, v[76:77]
	v_add_f32_e32 v78, v122, v78
	global_store_byte v[76:77], v80, off sc1
	v_add_f32_e32 v81, v115, v13
	s_mov_b32 s1, 0xc3e00000
	v_mov_b32_e32 v13, 0x43e00000
	global_store_byte v[76:77], v80, off offset:64 sc1
	v_mul_f32_e32 v76, 0x43000000, v78
	v_med3_f32 v76, v76, s1, v13
	v_mov_b32_e32 v80, v3
	v_cvt_pk_fp8_f32 v80, v76, 0
	v_mul_hi_i32_i24_e32 v77, 0x500, v74
	v_mul_i32_i24_e32 v76, 0x500, v74
	v_mul_f32_e32 v74, v5, v78
	v_mul_f32_e32 v82, 0x43000000, v81
	v_fma_f32 v74, v4, v81, -v74
	v_mul_f32_e32 v81, v5, v81
	v_med3_f32 v82, v82, s1, v13
	v_add_f32_e32 v74, v123, v74
	v_fmac_f32_e32 v81, v4, v78
	v_cvt_pk_fp8_f32 v83, v82, 0
	v_add_f32_e32 v78, v124, v81
	v_mul_f32_e32 v81, 0x43000000, v74
	v_med3_f32 v81, v81, s1, v13
	v_mov_b32_e32 v82, v3
	v_cvt_pk_fp8_f32 v82, v81, 0
	v_mul_f32_e32 v81, 0x43000000, v78
	v_med3_f32 v81, v81, s1, v13
	v_mov_b32_e32 v115, v3
	v_cvt_pk_fp8_f32 v83, 0, 0 op_sel:[0,0,1]
	v_cvt_pk_fp8_f32 v115, v81, 0
	v_cvt_pk_fp8_f32 v80, 0, 0 op_sel:[0,0,1]
	s_movk_i32 s0, 0x500
	v_lshl_add_u64 v[76:77], v[6:7], 0, v[76:77]
	v_cvt_pk_fp8_f32 v82, 0, 0 op_sel:[0,0,1]
	global_store_byte v[76:77], v83, off sc1
	global_store_byte v[76:77], v80, off offset:64 sc1
	v_cvt_pk_fp8_f32 v115, 0, 0 op_sel:[0,0,1]
	v_mad_i64_i32 v[76:77], s[6:7], v72, s0, v[6:7]
	v_mul_f32_e32 v72, v5, v78
	v_fma_f32 v72, v4, v74, -v72
	v_add_f32_e32 v72, v125, v72
	v_mul_f32_e32 v74, v5, v74
	global_store_byte v[76:77], v82, off sc1
	global_store_byte v[76:77], v115, off offset:64 sc1
	v_mul_f32_e32 v76, 0x43000000, v72
	v_fmac_f32_e32 v74, v4, v78
	v_med3_f32 v76, v76, s1, v13
	v_mov_b32_e32 v80, v3
	v_add_f32_e32 v74, v113, v74
	v_cvt_pk_fp8_f32 v80, v76, 0
	v_mul_f32_e32 v76, 0x43000000, v74
	v_med3_f32 v76, v76, s1, v13
	v_mov_b32_e32 v78, v3
	v_cvt_pk_fp8_f32 v78, v76, 0
	v_mul_hi_i32_i24_e32 v77, 0x500, v70
	v_mul_i32_i24_e32 v76, 0x500, v70
	v_mul_f32_e32 v70, v5, v74
	v_fma_f32 v70, v4, v72, -v70
	v_add_f32_e32 v70, v111, v70
	v_mul_f32_e32 v72, v5, v72
	v_fmac_f32_e32 v72, v4, v74
	v_mul_f32_e32 v74, 0x43000000, v70
	v_cvt_pk_fp8_f32 v80, 0, 0 op_sel:[0,0,1]
	v_add_f32_e32 v72, v109, v72
	v_med3_f32 v74, v74, s1, v13
	v_mov_b32_e32 v81, v3
	v_cvt_pk_fp8_f32 v78, 0, 0 op_sel:[0,0,1]
	v_cvt_pk_fp8_f32 v81, v74, 0
	v_mul_f32_e32 v74, 0x43000000, v72
	v_med3_f32 v74, v74, s1, v13
	v_mov_b32_e32 v82, v3
	v_lshl_add_u64 v[76:77], v[6:7], 0, v[76:77]
	v_cvt_pk_fp8_f32 v82, v74, 0
	global_store_byte v[76:77], v80, off sc1
	global_store_byte v[76:77], v78, off offset:64 sc1
	v_mad_i64_i32 v[76:77], s[6:7], v68, s0, v[6:7]
	v_mul_f32_e32 v68, v5, v72
	v_fma_f32 v68, v4, v70, -v68
	v_cvt_pk_fp8_f32 v81, 0, 0 op_sel:[0,0,1]
	v_add_f32_e32 v68, v114, v68
	v_mul_f32_e32 v70, v5, v70
	v_cvt_pk_fp8_f32 v82, 0, 0 op_sel:[0,0,1]
	v_fmac_f32_e32 v70, v4, v72
	v_mul_f32_e32 v72, 0x43000000, v68
	v_add_f32_e32 v70, v112, v70
	v_med3_f32 v72, v72, s1, v13
	v_mov_b32_e32 v74, v3
	v_cvt_pk_fp8_f32 v74, v72, 0
	v_mul_f32_e32 v72, 0x43000000, v70
; __device__ __forceinline__ void phase_carry(Frame& F, int l) {
;     ...
; #pragma unroll
;     for (int step = 0; step < 36; ++step) {
;         int inst; if (step < 4) inst = 256 + b * 4 + (d == 0 ? step : 3 - step); else inst = b * 32 + (d == 0 ? step - 4 : 35 - step);
;         const size_t row = (size_t)g * NINST + inst;
;         a8[row * KS2 + 1024 + d * 128 + p] = (unsigned char)(pk4_fp8(hr * S5_SH, 0.f, 0.f, 0.f) & 0xffu); a8[row * KS2 + 1024 + d * 128 + 64 + p] = (unsigned char)(pk4_fp8(hi * S5_SH, 0.f, 0.f, 0.f) & 0xffu);
;         const float nr = lt.x * hr - lt.y * hi + frv[step]; hi = lt.x * hi + lt.y * hr + fiv[step]; hr = nr; }
	global_store_byte v[76:77], v81, off sc1
	global_store_byte v[76:77], v82, off offset:64 sc1
	v_med3_f32 v72, v72, s1, v13
	v_mov_b32_e32 v78, v3
	v_mad_i64_i32 v[76:77], s[6:7], v66, s0, v[6:7]
	v_mul_f32_e32 v66, v5, v70
	v_cvt_pk_fp8_f32 v78, v72, 0
	v_fma_f32 v66, v4, v68, -v66
	v_add_f32_e32 v66, v110, v66
	v_mul_f32_e32 v68, v5, v68
	v_fmac_f32_e32 v68, v4, v70
	v_mul_f32_e32 v70, 0x43000000, v66
	v_cvt_pk_fp8_f32 v74, 0, 0 op_sel:[0,0,1]
	v_add_f32_e32 v68, v108, v68
	v_med3_f32 v70, v70, s1, v13
	v_mov_b32_e32 v72, v3
	v_cvt_pk_fp8_f32 v78, 0, 0 op_sel:[0,0,1]
	v_cvt_pk_fp8_f32 v72, v70, 0
	v_mul_f32_e32 v70, 0x43000000, v68
	v_med3_f32 v70, v70, s1, v13
	v_mov_b32_e32 v80, v3
	v_cvt_pk_fp8_f32 v80, v70, 0
	global_store_byte v[76:77], v74, off sc1
	global_store_byte v[76:77], v78, off offset:64 sc1
	v_mad_i64_i32 v[76:77], s[6:7], v64, s0, v[6:7]
	v_mul_f32_e32 v64, v5, v68
	v_fma_f32 v64, v4, v66, -v64
	v_cvt_pk_fp8_f32 v72, 0, 0 op_sel:[0,0,1]
	v_add_f32_e32 v64, v107, v64
	v_mul_f32_e32 v66, v5, v66
	v_cvt_pk_fp8_f32 v80, 0, 0 op_sel:[0,0,1]
	v_fmac_f32_e32 v66, v4, v68
	v_mul_f32_e32 v68, 0x43000000, v64
	v_add_f32_e32 v66, v105, v66
	v_med3_f32 v68, v68, s1, v13
	v_mov_b32_e32 v70, v3
	v_cvt_pk_fp8_f32 v70, v68, 0
	v_mul_f32_e32 v68, 0x43000000, v66
	global_store_byte v[76:77], v72, off sc1
	global_store_byte v[76:77], v80, off offset:64 sc1
	v_med3_f32 v68, v68, s1, v13
	v_mov_b32_e32 v72, v3
	v_mad_i64_i32 v[76:77], s[6:7], v62, s0, v[6:7]
	v_mul_f32_e32 v62, v5, v66
	v_cvt_pk_fp8_f32 v72, v68, 0
	v_fma_f32 v62, v4, v64, -v62
	v_add_f32_e32 v62, v103, v62
	v_mul_f32_e32 v64, v5, v64
	v_fmac_f32_e32 v64, v4, v66
	v_mul_f32_e32 v66, 0x43000000, v62
	v_cvt_pk_fp8_f32 v70, 0, 0 op_sel:[0,0,1]
	v_add_f32_e32 v64, v101, v64
	v_med3_f32 v66, v66, s1, v13
	v_mov_b32_e32 v68, v3
	v_cvt_pk_fp8_f32 v72, 0, 0 op_sel:[0,0,1]
	v_cvt_pk_fp8_f32 v68, v66, 0
	v_mul_f32_e32 v66, 0x43000000, v64
	v_med3_f32 v66, v66, s1, v13
	v_mov_b32_e32 v74, v3
	v_cvt_pk_fp8_f32 v74, v66, 0
	global_store_byte v[76:77], v70, off sc1
	global_store_byte v[76:77], v72, off offset:64 sc1
	v_mad_i64_i32 v[76:77], s[6:7], v60, s0, v[6:7]
	v_mul_f32_e32 v60, v5, v64
	v_fma_f32 v60, v4, v62, -v60
	v_cvt_pk_fp8_f32 v68, 0, 0 op_sel:[0,0,1]
	v_add_f32_e32 v60, v106, v60
	v_mul_f32_e32 v62, v5, v62
	v_cvt_pk_fp8_f32 v74, 0, 0 op_sel:[0,0,1]
	v_fmac_f32_e32 v62, v4, v64
	v_mul_f32_e32 v64, 0x43000000, v60
	v_add_f32_e32 v62, v104, v62
	v_med3_f32 v64, v64, s1, v13
	v_mov_b32_e32 v66, v3
	v_cvt_pk_fp8_f32 v66, v64, 0
	v_mul_f32_e32 v64, 0x43000000, v62
	global_store_byte v[76:77], v68, off sc1
	global_store_byte v[76:77], v74, off offset:64 sc1
	v_med3_f32 v64, v64, s1, v13
	v_mov_b32_e32 v68, v3
	v_mad_i64_i32 v[76:77], s[6:7], v58, s0, v[6:7]
	v_mul_f32_e32 v58, v5, v62
	v_cvt_pk_fp8_f32 v68, v64, 0
	v_fma_f32 v58, v4, v60, -v58
	v_add_f32_e32 v58, v102, v58
	v_mul_f32_e32 v60, v5, v60
	v_fmac_f32_e32 v60, v4, v62
	v_mul_f32_e32 v62, 0x43000000, v58
	v_cvt_pk_fp8_f32 v66, 0, 0 op_sel:[0,0,1]
	v_add_f32_e32 v60, v100, v60
	v_med3_f32 v62, v62, s1, v13
	v_mov_b32_e32 v64, v3
	v_cvt_pk_fp8_f32 v68, 0, 0 op_sel:[0,0,1]
	v_cvt_pk_fp8_f32 v64, v62, 0
	v_mul_f32_e32 v62, 0x43000000, v60
	v_med3_f32 v62, v62, s1, v13
	v_mov_b32_e32 v70, v3
	v_cvt_pk_fp8_f32 v70, v62, 0
	global_store_byte v[76:77], v66, off sc1
	global_store_byte v[76:77], v68, off offset:64 sc1
	v_mad_i64_i32 v[76:77], s[6:7], v56, s0, v[6:7]
	v_mul_f32_e32 v56, v5, v60
	v_fma_f32 v56, v4, v58, -v56
	v_cvt_pk_fp8_f32 v64, 0, 0 op_sel:[0,0,1]
	v_add_f32_e32 v56, v99, v56
	v_mul_f32_e32 v58, v5, v58
	v_cvt_pk_fp8_f32 v70, 0, 0 op_sel:[0,0,1]
	v_fmac_f32_e32 v58, v4, v60
	v_mul_f32_e32 v60, 0x43000000, v56
	v_add_f32_e32 v58, v97, v58
	v_med3_f32 v60, v60, s1, v13
	v_mov_b32_e32 v62, v3
	v_cvt_pk_fp8_f32 v62, v60, 0
	v_mul_f32_e32 v60, 0x43000000, v58
	global_store_byte v[76:77], v64, off sc1
	global_store_byte v[76:77], v70, off offset:64 sc1
	v_med3_f32 v60, v60, s1, v13
	v_mov_b32_e32 v64, v3
	v_mad_i64_i32 v[76:77], s[6:7], v54, s0, v[6:7]
	v_mul_f32_e32 v54, v5, v58
	v_cvt_pk_fp8_f32 v64, v60, 0
	v_fma_f32 v54, v4, v56, -v54
	v_add_f32_e32 v54, v95, v54
	v_mul_f32_e32 v56, v5, v56
	v_fmac_f32_e32 v56, v4, v58
	v_mul_f32_e32 v58, 0x43000000, v54
	v_cvt_pk_fp8_f32 v62, 0, 0 op_sel:[0,0,1]
	v_add_f32_e32 v56, v93, v56
	v_med3_f32 v58, v58, s1, v13
	v_mov_b32_e32 v60, v3
	v_cvt_pk_fp8_f32 v64, 0, 0 op_sel:[0,0,1]
	v_cvt_pk_fp8_f32 v60, v58, 0
	v_mul_f32_e32 v58, 0x43000000, v56
	v_med3_f32 v58, v58, s1, v13
	v_mov_b32_e32 v66, v3
	v_cvt_pk_fp8_f32 v66, v58, 0
	global_store_byte v[76:77], v62, off sc1
	global_store_byte v[76:77], v64, off offset:64 sc1
	v_mad_i64_i32 v[76:77], s[6:7], v52, s0, v[6:7]
	v_mul_f32_e32 v52, v5, v56
	v_fma_f32 v52, v4, v54, -v52
	v_cvt_pk_fp8_f32 v60, 0, 0 op_sel:[0,0,1]
	v_add_f32_e32 v52, v98, v52
	v_mul_f32_e32 v54, v5, v54
	v_cvt_pk_fp8_f32 v66, 0, 0 op_sel:[0,0,1]
	v_fmac_f32_e32 v54, v4, v56
	v_mul_f32_e32 v56, 0x43000000, v52
	v_add_f32_e32 v54, v96, v54
	v_med3_f32 v56, v56, s1, v13
	v_mov_b32_e32 v58, v3
	v_cvt_pk_fp8_f32 v58, v56, 0
	v_mul_f32_e32 v56, 0x43000000, v54
	global_store_byte v[76:77], v60, off sc1
	global_store_byte v[76:77], v66, off offset:64 sc1
	v_med3_f32 v56, v56, s1, v13
	v_mov_b32_e32 v60, v3
	v_mad_i64_i32 v[76:77], s[6:7], v50, s0, v[6:7]
	v_mul_f32_e32 v50, v5, v54
	v_cvt_pk_fp8_f32 v60, v56, 0
	v_fma_f32 v50, v4, v52, -v50
	v_add_f32_e32 v50, v94, v50
	v_mul_f32_e32 v52, v5, v52
	v_fmac_f32_e32 v52, v4, v54
	v_mul_f32_e32 v54, 0x43000000, v50
	v_cvt_pk_fp8_f32 v58, 0, 0 op_sel:[0,0,1]
	v_add_f32_e32 v52, v92, v52
	v_med3_f32 v54, v54, s1, v13
; __device__ __forceinline__ void phase_carry(Frame& F, int l) {
;     ...
; #pragma unroll
;     for (int step = 0; step < 36; ++step) {
;         int inst; if (step < 4) inst = 256 + b * 4 + (d == 0 ? step : 3 - step); else inst = b * 32 + (d == 0 ? step - 4 : 35 - step);
;         const size_t row = (size_t)g * NINST + inst;
;         a8[row * KS2 + 1024 + d * 128 + p] = (unsigned char)(pk4_fp8(hr * S5_SH, 0.f, 0.f, 0.f) & 0xffu); a8[row * KS2 + 1024 + d * 128 + 64 + p] = (unsigned char)(pk4_fp8(hi * S5_SH, 0.f, 0.f, 0.f) & 0xffu);
;         const float nr = lt.x * hr - lt.y * hi + frv[step]; hi = lt.x * hi + lt.y * hr + fiv[step]; hr = nr; }
	v_mov_b32_e32 v56, v3
	v_cvt_pk_fp8_f32 v60, 0, 0 op_sel:[0,0,1]
	v_cvt_pk_fp8_f32 v56, v54, 0
	v_mul_f32_e32 v54, 0x43000000, v52
	v_med3_f32 v54, v54, s1, v13
	v_mov_b32_e32 v62, v3
	v_cvt_pk_fp8_f32 v62, v54, 0
	global_store_byte v[76:77], v58, off sc1
	global_store_byte v[76:77], v60, off offset:64 sc1
	v_mad_i64_i32 v[76:77], s[6:7], v48, s0, v[6:7]
	v_mul_f32_e32 v48, v5, v52
	v_fma_f32 v48, v4, v50, -v48
	v_cvt_pk_fp8_f32 v56, 0, 0 op_sel:[0,0,1]
	v_add_f32_e32 v48, v91, v48
	v_mul_f32_e32 v50, v5, v50
	v_cvt_pk_fp8_f32 v62, 0, 0 op_sel:[0,0,1]
	v_fmac_f32_e32 v50, v4, v52
	v_mul_f32_e32 v52, 0x43000000, v48
	v_add_f32_e32 v50, v89, v50
	v_med3_f32 v52, v52, s1, v13
	v_mov_b32_e32 v54, v3
	v_cvt_pk_fp8_f32 v54, v52, 0
	v_mul_f32_e32 v52, 0x43000000, v50
	global_store_byte v[76:77], v56, off sc1
	global_store_byte v[76:77], v62, off offset:64 sc1
	v_med3_f32 v52, v52, s1, v13
	v_mov_b32_e32 v56, v3
	v_mad_i64_i32 v[76:77], s[6:7], v46, s0, v[6:7]
	v_mul_f32_e32 v46, v5, v50
	v_cvt_pk_fp8_f32 v56, v52, 0
	v_fma_f32 v46, v4, v48, -v46
	v_add_f32_e32 v46, v87, v46
	v_mul_f32_e32 v48, v5, v48
	v_fmac_f32_e32 v48, v4, v50
	v_mul_f32_e32 v50, 0x43000000, v46
	v_cvt_pk_fp8_f32 v54, 0, 0 op_sel:[0,0,1]
	v_add_f32_e32 v48, v85, v48
	v_med3_f32 v50, v50, s1, v13
	v_mov_b32_e32 v52, v3
	v_cvt_pk_fp8_f32 v56, 0, 0 op_sel:[0,0,1]
	v_cvt_pk_fp8_f32 v52, v50, 0
	v_mul_f32_e32 v50, 0x43000000, v48
	v_med3_f32 v50, v50, s1, v13
	v_mov_b32_e32 v58, v3
	v_cvt_pk_fp8_f32 v58, v50, 0
	global_store_byte v[76:77], v54, off sc1
	global_store_byte v[76:77], v56, off offset:64 sc1
	v_mad_i64_i32 v[76:77], s[6:7], v44, s0, v[6:7]
	v_mul_f32_e32 v44, v5, v48
	v_fma_f32 v44, v4, v46, -v44
	v_cvt_pk_fp8_f32 v52, 0, 0 op_sel:[0,0,1]
	v_add_f32_e32 v44, v90, v44
	v_mul_f32_e32 v46, v5, v46
	v_cvt_pk_fp8_f32 v58, 0, 0 op_sel:[0,0,1]
	v_fmac_f32_e32 v46, v4, v48
	v_mul_f32_e32 v48, 0x43000000, v44
	v_add_f32_e32 v46, v88, v46
	v_med3_f32 v48, v48, s1, v13
	v_mov_b32_e32 v50, v3
	v_cvt_pk_fp8_f32 v50, v48, 0
	v_mul_f32_e32 v48, 0x43000000, v46
	global_store_byte v[76:77], v52, off sc1
	global_store_byte v[76:77], v58, off offset:64 sc1
	v_med3_f32 v48, v48, s1, v13
	v_mov_b32_e32 v52, v3
	v_cvt_pk_fp8_f32 v52, v48, 0
	v_mad_i64_i32 v[76:77], s[6:7], v42, s0, v[6:7]
	v_mul_f32_e32 v42, v5, v46
	v_fma_f32 v42, v4, v44, -v42
	v_add_f32_e32 v42, v86, v42
	v_mul_f32_e32 v44, v5, v44
	v_cvt_pk_fp8_f32 v50, 0, 0 op_sel:[0,0,1]
	v_fmac_f32_e32 v44, v4, v46
	v_mul_f32_e32 v46, 0x43000000, v42
	v_cvt_pk_fp8_f32 v52, 0, 0 op_sel:[0,0,1]
	v_add_f32_e32 v44, v84, v44
	v_med3_f32 v46, v46, s1, v13
	v_mov_b32_e32 v48, v3
	v_cvt_pk_fp8_f32 v48, v46, 0
	v_mul_f32_e32 v46, 0x43000000, v44
	v_med3_f32 v46, v46, s1, v13
	v_mov_b32_e32 v54, v3
	v_cvt_pk_fp8_f32 v54, v46, 0
	global_store_byte v[76:77], v50, off sc1
	global_store_byte v[76:77], v52, off offset:64 sc1
	v_mad_i64_i32 v[76:77], s[6:7], v40, s0, v[6:7]
	v_mul_f32_e32 v40, v5, v44
	v_fma_f32 v40, v4, v42, -v40
	v_mul_f32_e32 v42, v5, v42
	v_fmac_f32_e32 v42, v4, v44
	v_cvt_pk_fp8_f32 v48, 0, 0 op_sel:[0,0,1]
	v_add_f32_e32 v40, v79, v40
	v_add_f32_e32 v42, v73, v42
	v_cvt_pk_fp8_f32 v54, 0, 0 op_sel:[0,0,1]
	v_mul_f32_e32 v44, 0x43000000, v40
	v_mad_i64_i32 v[72:73], s[6:7], v38, s0, v[6:7]
	v_mul_f32_e32 v38, v5, v42
	v_med3_f32 v44, v44, s1, v13
	v_mov_b32_e32 v46, v3
	v_fma_f32 v38, v4, v40, -v38
	v_cvt_pk_fp8_f32 v46, v44, 0
	v_mul_f32_e32 v44, 0x43000000, v42
	v_add_f32_e32 v38, v69, v38
	v_mul_f32_e32 v40, v5, v40
	global_store_byte v[76:77], v48, off sc1
	global_store_byte v[76:77], v54, off offset:64 sc1
	v_med3_f32 v44, v44, s1, v13
	v_mov_b32_e32 v48, v3
	v_fmac_f32_e32 v40, v4, v42
	v_mul_f32_e32 v42, 0x43000000, v38
	v_cvt_pk_fp8_f32 v48, v44, 0
	v_add_f32_e32 v40, v65, v40
	v_med3_f32 v42, v42, s1, v13
	v_mov_b32_e32 v44, v3
	v_cvt_pk_fp8_f32 v44, v42, 0
	v_mul_f32_e32 v42, 0x43000000, v40
	v_med3_f32 v42, v42, s1, v13
	v_mov_b32_e32 v50, v3
	v_cvt_pk_fp8_f32 v50, v42, 0
	v_cvt_pk_fp8_f32 v46, 0, 0 op_sel:[0,0,1]
	v_cvt_pk_fp8_f32 v44, 0, 0 op_sel:[0,0,1]
	v_mad_i64_i32 v[64:65], s[6:7], v36, s0, v[6:7]
	v_mul_f32_e32 v36, v5, v40
	v_cvt_pk_fp8_f32 v48, 0, 0 op_sel:[0,0,1]
	v_cvt_pk_fp8_f32 v50, 0, 0 op_sel:[0,0,1]
	v_fma_f32 v36, v4, v38, -v36
	v_mul_f32_e32 v38, v5, v38
	v_fmac_f32_e32 v38, v4, v40
	v_add_f32_e32 v36, v75, v36
	v_add_f32_e32 v38, v71, v38
	global_store_byte v[72:73], v46, off sc1
	global_store_byte v[72:73], v48, off offset:64 sc1
	global_store_byte v[64:65], v44, off sc1
	global_store_byte v[64:65], v50, off offset:64 sc1
	v_mul_f32_e32 v40, 0x43000000, v36
	v_mad_i64_i32 v[64:65], s[6:7], v34, s0, v[6:7]
	v_mul_f32_e32 v34, v5, v38
	v_med3_f32 v40, v40, s1, v13
	v_mov_b32_e32 v42, v3
	v_fma_f32 v34, v4, v36, -v34
	v_cvt_pk_fp8_f32 v42, v40, 0
	v_mul_f32_e32 v40, 0x43000000, v38
	v_add_f32_e32 v34, v67, v34
	v_mul_f32_e32 v36, v5, v36
	v_med3_f32 v40, v40, s1, v13
	v_mov_b32_e32 v44, v3
	v_fmac_f32_e32 v36, v4, v38
	v_mul_f32_e32 v38, 0x43000000, v34
	v_cvt_pk_fp8_f32 v44, v40, 0
	v_add_f32_e32 v36, v63, v36
	v_med3_f32 v38, v38, s1, v13
	v_mov_b32_e32 v40, v3
	v_cvt_pk_fp8_f32 v40, v38, 0
	v_mul_f32_e32 v38, 0x43000000, v36
	v_med3_f32 v38, v38, s1, v13
	v_mov_b32_e32 v46, v3
	v_cvt_pk_fp8_f32 v46, v38, 0
	v_mad_i64_i32 v[62:63], s[6:7], v32, s0, v[6:7]
	v_mul_f32_e32 v32, v5, v36
	v_fma_f32 v32, v4, v34, -v32
	v_mul_f32_e32 v34, v5, v34
	v_fmac_f32_e32 v34, v4, v36
	v_cvt_pk_fp8_f32 v42, 0, 0 op_sel:[0,0,1]
	v_cvt_pk_fp8_f32 v40, 0, 0 op_sel:[0,0,1]
	v_add_f32_e32 v32, v61, v32
	v_add_f32_e32 v34, v57, v34
	v_cvt_pk_fp8_f32 v44, 0, 0 op_sel:[0,0,1]
	v_cvt_pk_fp8_f32 v46, 0, 0 op_sel:[0,0,1]
; __device__ __forceinline__ void phase_carry(Frame& F, int l) {
;     ...
; #pragma unroll
;     for (int step = 0; step < 36; ++step) {
;         int inst; if (step < 4) inst = 256 + b * 4 + (d == 0 ? step : 3 - step); else inst = b * 32 + (d == 0 ? step - 4 : 35 - step);
;         const size_t row = (size_t)g * NINST + inst;
;         a8[row * KS2 + 1024 + d * 128 + p] = (unsigned char)(pk4_fp8(hr * S5_SH, 0.f, 0.f, 0.f) & 0xffu); a8[row * KS2 + 1024 + d * 128 + 64 + p] = (unsigned char)(pk4_fp8(hi * S5_SH, 0.f, 0.f, 0.f) & 0xffu);
;         const float nr = lt.x * hr - lt.y * hi + frv[step]; hi = lt.x * hi + lt.y * hr + fiv[step]; hr = nr; }
	v_mul_f32_e32 v36, 0x43000000, v32
	v_mad_i64_i32 v[56:57], s[6:7], v30, s0, v[6:7]
	v_mul_f32_e32 v30, v5, v34
	v_med3_f32 v36, v36, s1, v13
	v_mov_b32_e32 v38, v3
	v_fma_f32 v30, v4, v32, -v30
	v_cvt_pk_fp8_f32 v38, v36, 0
	v_mul_f32_e32 v36, 0x43000000, v34
	v_add_f32_e32 v30, v53, v30
	v_mul_f32_e32 v32, v5, v32
	global_store_byte v[64:65], v42, off sc1
	global_store_byte v[64:65], v44, off offset:64 sc1
	global_store_byte v[62:63], v40, off sc1
	global_store_byte v[62:63], v46, off offset:64 sc1
	v_med3_f32 v36, v36, s1, v13
	v_mov_b32_e32 v40, v3
	v_fmac_f32_e32 v32, v4, v34
	v_mul_f32_e32 v34, 0x43000000, v30
	v_cvt_pk_fp8_f32 v40, v36, 0
	v_add_f32_e32 v32, v49, v32
	v_med3_f32 v34, v34, s1, v13
	v_mov_b32_e32 v36, v3
	v_cvt_pk_fp8_f32 v36, v34, 0
	v_mul_f32_e32 v34, 0x43000000, v32
	v_med3_f32 v34, v34, s1, v13
	v_mov_b32_e32 v42, v3
	v_cvt_pk_fp8_f32 v42, v34, 0
	v_cvt_pk_fp8_f32 v38, 0, 0 op_sel:[0,0,1]
	v_cvt_pk_fp8_f32 v36, 0, 0 op_sel:[0,0,1]
	v_mad_i64_i32 v[48:49], s[6:7], v28, s0, v[6:7]
	v_mul_f32_e32 v28, v5, v32
	v_cvt_pk_fp8_f32 v40, 0, 0 op_sel:[0,0,1]
	v_cvt_pk_fp8_f32 v42, 0, 0 op_sel:[0,0,1]
	v_fma_f32 v28, v4, v30, -v28
	v_mul_f32_e32 v30, v5, v30
	v_fmac_f32_e32 v30, v4, v32
	v_add_f32_e32 v28, v59, v28
	v_add_f32_e32 v30, v55, v30
	global_store_byte v[56:57], v38, off sc1
	global_store_byte v[56:57], v40, off offset:64 sc1
	global_store_byte v[48:49], v36, off sc1
	global_store_byte v[48:49], v42, off offset:64 sc1
	v_mul_f32_e32 v32, 0x43000000, v28
	v_mad_i64_i32 v[48:49], s[6:7], v26, s0, v[6:7]
	v_mul_f32_e32 v26, v5, v30
	v_med3_f32 v32, v32, s1, v13
	v_mov_b32_e32 v34, v3
	v_fma_f32 v26, v4, v28, -v26
	v_cvt_pk_fp8_f32 v34, v32, 0
	v_mul_f32_e32 v32, 0x43000000, v30
	v_add_f32_e32 v26, v51, v26
	v_mul_f32_e32 v28, v5, v28
	v_med3_f32 v32, v32, s1, v13
	v_mov_b32_e32 v36, v3
	v_fmac_f32_e32 v28, v4, v30
	v_mul_f32_e32 v30, 0x43000000, v26
	v_cvt_pk_fp8_f32 v36, v32, 0
	v_add_f32_e32 v28, v47, v28
	v_med3_f32 v30, v30, s1, v13
	v_mov_b32_e32 v32, v3
	v_cvt_pk_fp8_f32 v32, v30, 0
	v_mul_f32_e32 v30, 0x43000000, v28
	v_med3_f32 v30, v30, s1, v13
	v_mov_b32_e32 v38, v3
	v_cvt_pk_fp8_f32 v38, v30, 0
	v_mad_i64_i32 v[46:47], s[6:7], v24, s0, v[6:7]
	v_mul_f32_e32 v24, v5, v28
	v_fma_f32 v24, v4, v26, -v24
	v_mul_f32_e32 v26, v5, v26
	v_cvt_pk_fp8_f32 v34, 0, 0 op_sel:[0,0,1]
	v_cvt_pk_fp8_f32 v32, 0, 0 op_sel:[0,0,1]
	v_add_f32_e32 v24, v45, v24
	v_fmac_f32_e32 v26, v4, v28
	v_cvt_pk_fp8_f32 v36, 0, 0 op_sel:[0,0,1]
	v_cvt_pk_fp8_f32 v38, 0, 0 op_sel:[0,0,1]
	v_add_f32_e32 v26, v41, v26
	v_mul_f32_e32 v28, 0x43000000, v24
	v_med3_f32 v28, v28, s1, v13
	v_mov_b32_e32 v30, v3
	v_mad_i64_i32 v[40:41], s[6:7], v22, s0, v[6:7]
	v_mul_f32_e32 v22, v5, v26
	v_cvt_pk_fp8_f32 v30, v28, 0
	v_mul_f32_e32 v28, 0x43000000, v26
	v_fma_f32 v22, v4, v24, -v22
	global_store_byte v[48:49], v34, off sc1
	global_store_byte v[48:49], v36, off offset:64 sc1
	global_store_byte v[46:47], v32, off sc1
	global_store_byte v[46:47], v38, off offset:64 sc1
	v_med3_f32 v28, v28, s1, v13
	v_mov_b32_e32 v32, v3
	v_add_f32_e32 v22, v37, v22
	v_mul_f32_e32 v24, v5, v24
	v_cvt_pk_fp8_f32 v32, v28, 0
	v_fmac_f32_e32 v24, v4, v26
	v_mul_f32_e32 v26, 0x43000000, v22
	v_add_f32_e32 v24, v33, v24
	v_med3_f32 v26, v26, s1, v13
	v_mov_b32_e32 v28, v3
	v_cvt_pk_fp8_f32 v28, v26, 0
	v_mul_f32_e32 v26, 0x43000000, v24
	v_cvt_pk_fp8_f32 v30, 0, 0 op_sel:[0,0,1]
	v_med3_f32 v26, v26, s1, v13
	v_mov_b32_e32 v34, v3
	v_cvt_pk_fp8_f32 v32, 0, 0 op_sel:[0,0,1]
	v_cvt_pk_fp8_f32 v34, v26, 0
	global_store_byte v[40:41], v30, off sc1
	global_store_byte v[40:41], v32, off offset:64 sc1
	v_cvt_pk_fp8_f32 v28, 0, 0 op_sel:[0,0,1]
	v_mad_i64_i32 v[32:33], s[6:7], v20, s0, v[6:7]
	v_mul_f32_e32 v20, v5, v24
	v_cvt_pk_fp8_f32 v34, 0, 0 op_sel:[0,0,1]
	v_fma_f32 v20, v4, v22, -v20
	v_mul_f32_e32 v22, v5, v22
	v_fmac_f32_e32 v22, v4, v24
	v_add_f32_e32 v20, v43, v20
	v_add_f32_e32 v22, v39, v22
	global_store_byte v[32:33], v28, off sc1
	global_store_byte v[32:33], v34, off offset:64 sc1
	v_mul_f32_e32 v24, 0x43000000, v20
	v_mad_i64_i32 v[32:33], s[6:7], v18, s0, v[6:7]
	v_mul_f32_e32 v18, v5, v22
	v_med3_f32 v24, v24, s1, v13
	v_mov_b32_e32 v26, v3
	v_fma_f32 v18, v4, v20, -v18
	v_cvt_pk_fp8_f32 v26, v24, 0
	v_mul_f32_e32 v24, 0x43000000, v22
	v_add_f32_e32 v18, v35, v18
	v_mul_f32_e32 v20, v5, v20
	v_med3_f32 v24, v24, s1, v13
	v_mov_b32_e32 v28, v3
	v_fmac_f32_e32 v20, v4, v22
	v_mul_f32_e32 v22, 0x43000000, v18
	v_cvt_pk_fp8_f32 v28, v24, 0
; __device__ __forceinline__ void phase_carry(Frame& F, int l) {
;     ...
; #pragma unroll
;     for (int step = 0; step < 36; ++step) {
;         int inst; if (step < 4) inst = 256 + b * 4 + (d == 0 ? step : 3 - step); else inst = b * 32 + (d == 0 ? step - 4 : 35 - step);
;         const size_t row = (size_t)g * NINST + inst;
;         a8[row * KS2 + 1024 + d * 128 + p] = (unsigned char)(pk4_fp8(hr * S5_SH, 0.f, 0.f, 0.f) & 0xffu); a8[row * KS2 + 1024 + d * 128 + 64 + p] = (unsigned char)(pk4_fp8(hi * S5_SH, 0.f, 0.f, 0.f) & 0xffu);
;         const float nr = lt.x * hr - lt.y * hi + frv[step]; hi = lt.x * hi + lt.y * hr + fiv[step]; hr = nr; }
	v_add_f32_e32 v20, v31, v20
	v_med3_f32 v22, v22, s1, v13
	v_mov_b32_e32 v24, v3
	v_cvt_pk_fp8_f32 v24, v22, 0
	v_mul_f32_e32 v22, 0x43000000, v20
	v_med3_f32 v22, v22, s1, v13
	v_mov_b32_e32 v34, v3
	v_cvt_pk_fp8_f32 v26, 0, 0 op_sel:[0,0,1]
	v_cvt_pk_fp8_f32 v34, v22, 0
	v_mad_i64_i32 v[30:31], s[6:7], v16, s0, v[6:7]
	v_mul_f32_e32 v16, v5, v20
	v_cvt_pk_fp8_f32 v28, 0, 0 op_sel:[0,0,1]
	v_fma_f32 v16, v4, v18, -v16
	v_mul_f32_e32 v18, v5, v18
	v_fmac_f32_e32 v18, v4, v20
	v_cvt_pk_fp8_f32 v24, 0, 0 op_sel:[0,0,1]
	v_add_f32_e32 v16, v29, v16
	v_add_f32_e32 v18, v27, v18
	global_store_byte v[32:33], v26, off sc1
	global_store_byte v[32:33], v28, off offset:64 sc1
	v_cvt_pk_fp8_f32 v34, 0, 0 op_sel:[0,0,1]
	v_mul_f32_e32 v20, 0x43000000, v16
	v_mad_i64_i32 v[26:27], s[6:7], v14, s0, v[6:7]
	v_mul_f32_e32 v14, v5, v18
	v_med3_f32 v20, v20, s1, v13
	v_mov_b32_e32 v22, v3
	v_fma_f32 v14, v4, v16, -v14
	v_cvt_pk_fp8_f32 v22, v20, 0
	v_mul_f32_e32 v20, 0x43000000, v18
	v_add_f32_e32 v14, v21, v14
	v_mul_f32_e32 v16, v5, v16
	global_store_byte v[30:31], v24, off sc1
	global_store_byte v[30:31], v34, off offset:64 sc1
	v_med3_f32 v20, v20, s1, v13
	v_mov_b32_e32 v24, v3
	v_fmac_f32_e32 v16, v4, v18
	v_mul_f32_e32 v18, 0x43000000, v14
	v_cvt_pk_fp8_f32 v24, v20, 0
	v_add_f32_e32 v16, v19, v16
	v_med3_f32 v18, v18, s1, v13
	v_mov_b32_e32 v20, v3
	v_cvt_pk_fp8_f32 v20, v18, 0
	v_mul_f32_e32 v18, 0x43000000, v16
	v_med3_f32 v18, v18, s1, v13
	v_mov_b32_e32 v21, v3
	v_cvt_pk_fp8_f32 v21, v18, 0
	v_cvt_pk_fp8_f32 v22, 0, 0 op_sel:[0,0,1]
	v_cvt_pk_fp8_f32 v20, 0, 0 op_sel:[0,0,1]
	v_mad_i64_i32 v[18:19], s[6:7], v12, s0, v[6:7]
	v_mul_f32_e32 v12, v5, v16
	v_cvt_pk_fp8_f32 v24, 0, 0 op_sel:[0,0,1]
	v_cvt_pk_fp8_f32 v21, 0, 0 op_sel:[0,0,1]
	v_fma_f32 v12, v4, v14, -v12
	v_mul_f32_e32 v14, v5, v14
	v_fmac_f32_e32 v14, v4, v16
	v_add_f32_e32 v12, v25, v12
	v_add_f32_e32 v14, v23, v14
	global_store_byte v[26:27], v22, off sc1
	global_store_byte v[26:27], v24, off offset:64 sc1
	global_store_byte v[18:19], v20, off sc1
	global_store_byte v[18:19], v21, off offset:64 sc1
	v_mul_f32_e32 v16, 0x43000000, v12
	v_mad_i64_i32 v[18:19], s[6:7], v10, s0, v[6:7]
	v_mul_f32_e32 v10, v5, v14
	v_med3_f32 v16, v16, s1, v13
	v_mov_b32_e32 v20, v3
	v_fma_f32 v10, v4, v12, -v10
	v_cvt_pk_fp8_f32 v20, v16, 0
	v_mul_f32_e32 v16, 0x43000000, v14
	v_add_f32_e32 v10, v17, v10
	v_mul_f32_e32 v12, v5, v12
	v_med3_f32 v16, v16, s1, v13
	v_mov_b32_e32 v21, v3
	v_fmac_f32_e32 v12, v4, v14
	v_mul_f32_e32 v14, 0x43000000, v10
	v_cvt_pk_fp8_f32 v21, v16, 0
	v_add_f32_e32 v12, v15, v12
	v_med3_f32 v14, v14, s1, v13
	v_mov_b32_e32 v16, v3
	v_cvt_pk_fp8_f32 v16, v14, 0
	v_mul_f32_e32 v14, 0x43000000, v12
	v_med3_f32 v14, v14, s1, v13
	v_mov_b32_e32 v17, v3
	v_cvt_pk_fp8_f32 v17, v14, 0
	v_mad_i64_i32 v[14:15], s[6:7], v8, s0, v[6:7]
	v_mul_f32_e32 v8, v5, v12
	v_fma_f32 v8, v4, v10, -v8
	v_mul_f32_e32 v5, v5, v10
	v_add_f32_e32 v8, v11, v8
	v_fmac_f32_e32 v5, v4, v12
	v_add_f32_e32 v4, v9, v5
	v_mul_f32_e32 v8, 0x43000000, v8
	v_med3_f32 v8, v8, s1, v13
	v_mov_b32_e32 v9, v3
	v_mul_f32_e32 v4, 0x43000000, v4
	v_cvt_pk_fp8_f32 v9, v8, 0
	v_med3_f32 v4, v4, s1, v13
	v_cvt_pk_fp8_f32 v3, v4, 0
	v_cvt_pk_fp8_f32 v20, 0, 0 op_sel:[0,0,1]
	v_cvt_pk_fp8_f32 v16, 0, 0 op_sel:[0,0,1]
	v_cndmask_b32_e64 v5, 0, 31, vcc
	v_cvt_pk_fp8_f32 v9, 0, 0 op_sel:[0,0,1]
	v_cvt_pk_fp8_f32 v21, 0, 0 op_sel:[0,0,1]
	v_cvt_pk_fp8_f32 v17, 0, 0 op_sel:[0,0,1]
	v_or_b32_e32 v1, v1, v5
	v_cvt_pk_fp8_f32 v3, 0, 0 op_sel:[0,0,1]
	v_add_u32_e32 v1, v1, v2
	v_mad_i64_i32 v[4:5], s[0:1], v1, s0, v[6:7]
	global_store_byte v[18:19], v20, off sc1
	global_store_byte v[18:19], v21, off offset:64 sc1
	global_store_byte v[14:15], v16, off sc1
	global_store_byte v[14:15], v17, off offset:64 sc1
	global_store_byte v[4:5], v9, off sc1
	global_store_byte v[4:5], v3, off offset:64 sc1
.Lfd0_481:
	s_or_b64 exec, exec, s[4:5]
	s_waitcnt vmcnt(0) lgkmcnt(0)
	v_readlane_b32 s0, v254, 0
	v_readlane_b32 s1, v254, 1
	v_readlane_b32 s2, v254, 2
	v_readlane_b32 s3, v254, 3
	v_readlane_b32 s4, v254, 4
	v_readlane_b32 s5, v254, 5
	v_readlane_b32 s6, v254, 6
	v_readlane_b32 s7, v254, 7
	v_readlane_b32 s33, v254, 8
	v_readlane_b32 s38, v254, 9
	s_barrier
	v_cmp_eq_u32_e64 s[98:99], 0, v0
	s_and_saveexec_b64 s[100:101], s[98:99]
	s_cbranch_execz .Lfs0_pw
	v_mov_b32_e32 v2, s38
	v_mov_b32_e32 v3, s39
	v_mov_b32_e32 v4, 1
	flat_atomic_add v[2:3], v4 offset:3848
	s_waitcnt vmcnt(0) lgkmcnt(0)

; #define LAS __attribute__((address_space(3)))
; __device__ __forceinline__ unsigned xb_add(unsigned* p, unsigned v) { return __hip_atomic_fetch_add(p, v, __ATOMIC_RELAXED, __HIP_MEMORY_SCOPE_AGENT); }
; __device__ __forceinline__ unsigned xb_xcc_id() { return (unsigned)__builtin_amdgcn_s_getreg((3 << 11) | 20) & 0xFu; }
; __device__ __forceinline__ void xcd_barrier(const XcdBarrier& b) {
;     asm volatile("s_waitcnt vmcnt(0)" ::: "memory");
;     __syncthreads();
;     if (threadIdx.x == 0) {
;         unsigned* bar = b.bar;
;         __builtin_amdgcn_s_waitcnt(0);
;         unsigned nloc = b.st[0], nx = b.st[1];
;         if (nloc == 0u) { xcd_barrier_complete(bar, b.x, nloc, nx); b.st[0] = nloc; b.st[1] = nx; }
;         const unsigned old = xb_add(&bar[XB_XSUB(b.x)], 1u);
; __device__ __forceinline__ void grid_seam(Frame& F) {
;     XcdBarrier b; b.bar = (unsigned*)(F.ws + WS_CTL) + CW_BAR; b.x = xb_xcc_id(); b.st = (volatile LAS unsigned*)(F.lds + MISC_OFF) + 8;
;     xcd_barrier(b);
; }
.Lfd0_done:
	s_branch .Lfs0_end
	s_getreg_b32 s0, hwreg(HW_REG_XCC_ID, 0, 4)
	s_waitcnt vmcnt(0)
	s_waitcnt vmcnt(0)
	s_barrier
	s_mov_b64 s[2:3], exec
	v_readlane_b32 s4, v249, 3
	v_readlane_b32 s5, v249, 4
	s_and_b64 s[4:5], s[2:3], s[4:5]
	s_xor_b64 s[2:3], s[4:5], s[2:3]
	s_mov_b64 exec, s[4:5]
	s_cbranch_execz .LBB0_477
	s_add_i32 s1, 0, 0x20160
	v_mov_b32_e32 v1, s1
	s_waitcnt vmcnt(0) expcnt(0) lgkmcnt(0)
	ds_read_b32 v4, v1
	s_add_i32 s1, 0, 0x20164
	v_mov_b32_e32 v1, s1
	ds_read_b32 v2, v1
	s_and_b32 s41, s0, 15
	s_waitcnt lgkmcnt(1)
	v_cmp_ne_u32_e32 vcc, 0, v4
	s_cbranch_vccnz .LBB0_447
	v_readlane_b32 s6, v249, 0
	v_readlane_b32 s7, v249, 1
	s_load_dword s4, s[6:7], 0x14
	s_load_dwordx2 s[0:1], s[6:7], 0x4
	s_mov_b32 s23, 1
	s_waitcnt lgkmcnt(0)
	s_lshr_b32 s6, s4, 16
	s_and_b32 s4, s4, 0xffff
	s_cmp_lg_u32 s4, 0
	s_cselect_b64 s[4:5], -1, 0
	s_cmp_lg_u64 s[4:5], 0
	s_addc_u32 s0, s0, 0
	s_cmp_lg_u32 s6, 0
	s_cselect_b64 s[4:5], -1, 0
	s_cmp_lg_u64 s[4:5], 0
	s_mul_i32 s22, s0, s54
	s_addc_u32 s0, s1, 0
	s_add_u32 s4, s38, 0x4200
	s_addc_u32 s5, s39, 0
	s_add_u32 s6, s38, 0x4400
	s_addc_u32 s7, s39, 0
	s_add_u32 s8, s38, 0x4500
	s_addc_u32 s9, s39, 0
	s_add_u32 s10, s38, 0x4600
	s_addc_u32 s11, s39, 0
	s_add_u32 s12, s38, 0x4700
	s_addc_u32 s13, s39, 0
	s_add_u32 s14, s38, 0x4800
	s_addc_u32 s15, s39, 0
	s_add_u32 s16, s38, 0x4900
	s_addc_u32 s17, s39, 0
	s_add_u32 s18, s38, 0x4a00
	s_addc_u32 s19, s39, 0
	s_add_u32 s20, s38, 0x4b00
	s_addc_u32 s21, s39, 0
	s_add_u32 s24, s38, 0x4c00
	s_addc_u32 s25, s39, 0
	s_add_u32 s26, s38, 0x4d00
	s_addc_u32 s27, s39, 0
	s_add_u32 s28, s38, 0x4e00
	s_addc_u32 s29, s39, 0
	s_add_u32 s30, s38, 0x4f00
	s_addc_u32 s31, s39, 0
	s_add_u32 s34, s38, 0x5000
	s_addc_u32 s35, s39, 0
	s_add_u32 s36, s38, 0x5100
	s_addc_u32 s37, s39, 0
	s_add_u32 s42, s38, 0x5200
	s_addc_u32 s43, s39, 0
	s_add_u32 s44, s38, 0x5300
	s_addc_u32 s45, s39, 0
	s_mul_i32 s22, s22, s0
	s_mov_b64 s[0:1], 0
	v_mov_b64_e32 v[2:3], s[6:7]
	v_mov_b64_e32 v[4:5], s[8:9]
	v_mov_b64_e32 v[6:7], s[10:11]
	v_mov_b64_e32 v[8:9], s[12:13]
	v_mov_b64_e32 v[10:11], s[14:15]
	v_mov_b64_e32 v[12:13], s[16:17]
	v_mov_b64_e32 v[14:15], s[18:19]
	v_mov_b64_e32 v[16:17], s[20:21]
	v_mov_b64_e32 v[18:19], s[24:25]
	v_mov_b64_e32 v[20:21], s[26:27]
	v_mov_b64_e32 v[22:23], s[28:29]
	v_mov_b64_e32 v[24:25], s[30:31]
	v_mov_b64_e32 v[26:27], s[34:35]
	v_mov_b64_e32 v[28:29], s[36:37]
	v_mov_b64_e32 v[30:31], s[42:43]
	v_mov_b64_e32 v[32:33], s[44:45]
	s_branch .LBB0_437

; __device__ __forceinline__ void launder(Frame& F) { F.ws = opaque_ptr(F.ws); F.out = opaque_ptr(F.out);
;     int t = F.tid; asm volatile("" : "+v"(t)); F.tid = t; F.lane = t & 63; F.wave = __builtin_amdgcn_readfirstlane(t >> 6);
;     int g = gridDim.x, bx = blockIdx.x; asm volatile("" : "+v"(g), "+v"(bx)); g = __builtin_amdgcn_readfirstlane(g); bx = __builtin_amdgcn_readfirstlane(bx);
;     F.G = g; F.vcu = (g % 8 == 0) ? (bx % 8) * (g / 8) + bx / 8 : bx; }
.Lfs0_end:
	v_mov_b32_e32 v1, s38
	v_mov_b32_e32 v2, s39
	s_waitcnt lgkmcnt(0)
	s_barrier
	s_nop 0
	v_readfirstlane_b32 s2, v1
	v_readfirstlane_b32 s3, v2
	v_mov_b32_e32 v1, s33
	v_mov_b32_e32 v2, s40
	s_nop 0
	v_readfirstlane_b32 s33, v1
	v_readfirstlane_b32 s38, v2
	s_branch .Lfd0_end
	v_mov_b32_e32 v1, s54
	v_mov_b32_e32 v2, s95
	s_nop 0
	v_readfirstlane_b32 s1, v1
	s_and_b32 s0, s1, 7
	s_cmp_eq_u32 s0, 0
	v_readfirstlane_b32 s0, v2
	s_cbranch_scc0 .LBB0_479
	s_ashr_i32 s4, s0, 31
	s_lshr_b32 s4, s4, 29
	s_add_i32 s4, s0, s4
	s_ashr_i32 s5, s4, 3
	s_and_b32 s4, s4, -8
	s_ashr_i32 s1, s1, 3
	s_sub_i32 s0, s0, s4
	s_mul_i32 s0, s0, s1
	s_add_i32 s0, s0, s5

; __device__ __forceinline__ void wait_ctx_rows(Frame& F) {
;     if (F.wave == 0) { unsigned* cnt = (unsigned*)(F.ws + WS_CTL) + CW_CTXROWS; unsigned sp = 0;
;         while ((unsigned)__builtin_amdgcn_readfirstlane((int)__hip_atomic_load(cnt, __ATOMIC_RELAXED, __HIP_MEMORY_SCOPE_AGENT)) < (unsigned)MC) { __builtin_amdgcn_s_sleep(2); if (++sp > (1u << 22)) break; }
;         __builtin_amdgcn_fence(__ATOMIC_ACQUIRE, "agent");
;         asm volatile("s_waitcnt vmcnt(0)" ::: "memory"); }
;     __syncthreads();
.Lfd0_end:
	v_cmp_eq_u32_e64 s[98:99], 0, v0
	s_and_saveexec_b64 s[100:101], s[98:99]
	s_cbranch_execz .Lfs0_w
	v_mov_b32_e32 v2, s2
	v_mov_b32_e32 v3, s3
	s_mov_b32 s98, 0
.Lfs0_poll:
	flat_load_dword v4, v[2:3] offset:3848 sc1
	s_waitcnt vmcnt(0) lgkmcnt(0)
	v_readfirstlane_b32 s99, v4
	s_add_u32 s98, s98, 1
	s_cmp_ge_u32 s99, 64
	s_cbranch_scc1 .Lfs0_go
	s_sleep 2
	s_cmp_lt_u32 s98, 0x4000
	s_cbranch_scc1 .Lfs0_poll

; __device__ __forceinline__ void launder(Frame& F) { F.ws = opaque_ptr(F.ws); F.out = opaque_ptr(F.out);
;     int t = F.tid; asm volatile("" : "+v"(t)); F.tid = t; F.lane = t & 63; F.wave = __builtin_amdgcn_readfirstlane(t >> 6);
;     int g = gridDim.x, bx = blockIdx.x; asm volatile("" : "+v"(g), "+v"(bx)); g = __builtin_amdgcn_readfirstlane(g); bx = __builtin_amdgcn_readfirstlane(bx);
;     F.G = g; F.vcu = (g % 8 == 0) ? (bx % 8) * (g / 8) + bx / 8 : bx; }
.Lfs0_w:
	s_or_b64 exec, exec, s[100:101]
	v_mov_b32_e32 v1, s2
	v_mov_b32_e32 v2, s3
	s_waitcnt lgkmcnt(0)
	s_barrier
	s_nop 0
	v_readfirstlane_b32 s47, v1
	v_readfirstlane_b32 s48, v2
	v_mov_b32_e32 v1, s33
	v_mov_b32_e32 v2, s38
	s_nop 0
	v_readfirstlane_b32 s33, v1
	v_readfirstlane_b32 s46, v2
	v_mov_b32_e32 v1, s54
	v_mov_b32_e32 v2, s95
	s_nop 0
	v_readfirstlane_b32 s37, v1
	s_and_b32 s0, s37, 7
	s_cmp_eq_u32 s0, 0
	v_readfirstlane_b32 s49, v2
	s_cbranch_scc0 .LBB0_528
	s_ashr_i32 s1, s49, 31
	s_lshr_b32 s1, s1, 29
	s_add_i32 s1, s49, s1
	s_ashr_i32 s2, s1, 3
	s_and_b32 s1, s1, -8
	s_ashr_i32 s0, s37, 3
	s_sub_i32 s1, s49, s1
	s_mul_i32 s0, s1, s0
	s_add_i32 s49, s0, s2

; #define GAS __attribute__((address_space(1)))
; __device__ __forceinline__ void phase_carry(Frame& F, int l) {
;     const int gt = F.vcu * 512 + F.tid; if (gt >= NB * NG * 2 * SP) return;
;     const int p = gt & 63, d = (gt >> 6) & 1, g = (gt >> 7) & 31, b = gt >> 12;
;     const f32x2 lt = WSP(f32x2, WS_LT)[((l * NG + g) * 2 + d) * 64 + p];
;     const float* Fb = WSP(float, WS_F); unsigned char* a8 = WSP(unsigned char, WS_A8);
;     float hr = 0.f, hi = 0.f;
;     float frv[36], fiv[36];
; #pragma unroll
;     for (int step = 0; step < 36; ++step) {
;         int inst; if (step < 4) inst = 256 + b * 4 + (d == 0 ? step : 3 - step); else inst = b * 32 + (d == 0 ? step - 4 : 35 - step);
;         const size_t row = (size_t)g * NINST + inst;
;         frv[step] = *(const GAS float*)(Fb + row * 256 + d * 128 + p); fiv[step] = *(const GAS float*)(Fb + row * 256 + d * 128 + 64 + p); }
.Lfd1_1499:
	s_nop 0
	v_lshl_add_u32 v1, s0, 9, v0
	s_mov_b32 s0, 0x8000
	v_cmp_gt_i32_e32 vcc, s0, v1
	s_and_saveexec_b64 s[4:5], vcc
	s_cbranch_execz .Lfd1_1501
	v_bfe_u32 v17, v0, 6, 1
	v_bfe_u32 v7, v1, 7, 5
	v_and_b32_e32 v6, 63, v0
	v_ashrrev_i32_e32 v10, 12, v1
	v_lshlrev_b32_e32 v1, 7, v7
	v_lshlrev_b32_e32 v2, 6, v17
	v_or3_b32 v1, v1, v2, v6
	v_lshlrev_b32_e32 v2, 3, v1
	v_mov_b32_e32 v3, 0
	v_lshl_add_u64 v[4:5], s[2:3], 0, v[2:3]
	v_add_co_u32_e32 v4, vcc, 0x288000, v4
	v_lshlrev_b32_e32 v12, 2, v10
	s_nop 0
	v_addc_co_u32_e32 v5, vcc, 0, v5, vcc
	v_lshlrev_b32_e32 v8, 9, v17
	v_mov_b32_e32 v9, v3
	v_add_u32_e32 v14, 0x100, v12
	v_cmp_eq_u32_e32 vcc, 0, v17
	v_bfe_i32 v16, v0, 6, 1
	flat_load_dwordx2 v[4:5], v[4:5]
	v_lshl_add_u64 v[8:9], s[2:3], 0, v[8:9]
	s_mov_b64 s[0:1], 0x56900000
	v_lshlrev_b32_e32 v1, 5, v10
	v_or_b32_e32 v10, v17, v14
	v_sub_u32_e32 v12, v12, v17
	v_cndmask_b32_e64 v15, 0, 3, vcc
	v_lshl_add_u64 v[80:81], v[8:9], 0, s[0:1]
	v_and_or_b32 v8, v16, 3, v14
	v_add_u32_e32 v10, 1, v10
	v_add_u32_e32 v12, 0x102, v12
	v_or_b32_e32 v14, v14, v15
	v_lshlrev_b32_e32 v2, 9, v7
	v_ashrrev_i32_e32 v9, 31, v8
	v_ashrrev_i32_e32 v11, 31, v10
	v_ashrrev_i32_e32 v13, 31, v12
	v_ashrrev_i32_e32 v15, 31, v14
	v_lshl_add_u64 v[78:79], v[8:9], 0, v[2:3]
	v_lshl_add_u64 v[74:75], v[10:11], 0, v[2:3]
	v_lshl_add_u64 v[72:73], v[12:13], 0, v[2:3]
	v_lshl_add_u64 v[70:71], v[14:15], 0, v[2:3]
	v_lshlrev_b64 v[8:9], 10, v[78:79]
	v_lshlrev_b64 v[10:11], 10, v[74:75]
	v_lshlrev_b64 v[12:13], 10, v[72:73]
	v_lshlrev_b64 v[14:15], 10, v[70:71]
	v_lshl_add_u64 v[8:9], v[80:81], 0, v[8:9]
	v_lshlrev_b32_e32 v82, 2, v6
	v_mov_b32_e32 v83, v3
	v_lshl_add_u64 v[10:11], v[80:81], 0, v[10:11]
	v_lshl_add_u64 v[12:13], v[80:81], 0, v[12:13]
	v_lshl_add_u64 v[14:15], v[80:81], 0, v[14:15]
	v_lshl_add_u64 v[8:9], v[8:9], 0, v[82:83]
	v_lshl_add_u64 v[10:11], v[10:11], 0, v[82:83]
	v_lshl_add_u64 v[12:13], v[12:13], 0, v[82:83]
	v_lshl_add_u64 v[14:15], v[14:15], 0, v[82:83]
	global_load_dword v115, v[8:9], off
	global_load_dword v122, v[8:9], off offset:256
	global_load_dword v123, v[10:11], off
	global_load_dword v124, v[10:11], off offset:256
	global_load_dword v125, v[12:13], off
	global_load_dword v113, v[12:13], off offset:256
	global_load_dword v111, v[14:15], off
	global_load_dword v109, v[14:15], off offset:256
	v_and_or_b32 v8, v16, 31, v1
	v_cndmask_b32_e64 v10, 30, 1, vcc
	v_cndmask_b32_e64 v12, 29, 2, vcc
	v_cndmask_b32_e64 v14, 28, 3, vcc
	v_ashrrev_i32_e32 v9, 31, v8
	v_or_b32_e32 v10, v1, v10
	v_or_b32_e32 v12, v1, v12
	v_or_b32_e32 v14, v1, v14
	v_lshl_add_u64 v[68:69], v[8:9], 0, v[2:3]
	v_ashrrev_i32_e32 v11, 31, v10
	v_ashrrev_i32_e32 v13, 31, v12
	v_ashrrev_i32_e32 v15, 31, v14
	v_lshlrev_b64 v[8:9], 10, v[68:69]
	v_lshl_add_u64 v[66:67], v[10:11], 0, v[2:3]
	v_lshl_add_u64 v[64:65], v[12:13], 0, v[2:3]
	v_lshl_add_u64 v[62:63], v[14:15], 0, v[2:3]
	v_lshl_add_u64 v[8:9], v[80:81], 0, v[8:9]
	v_lshlrev_b64 v[10:11], 10, v[66:67]
	v_lshlrev_b64 v[12:13], 10, v[64:65]
	v_lshlrev_b64 v[14:15], 10, v[62:63]
	v_lshl_add_u64 v[8:9], v[8:9], 0, v[82:83]
	v_lshl_add_u64 v[10:11], v[80:81], 0, v[10:11]
	v_lshl_add_u64 v[12:13], v[80:81], 0, v[12:13]
	v_lshl_add_u64 v[14:15], v[80:81], 0, v[14:15]
	v_lshl_add_u64 v[10:11], v[10:11], 0, v[82:83]
	v_lshl_add_u64 v[12:13], v[12:13], 0, v[82:83]
	v_lshl_add_u64 v[14:15], v[14:15], 0, v[82:83]
	global_load_dword v114, v[8:9], off
	global_load_dword v112, v[8:9], off offset:256
	global_load_dword v110, v[10:11], off
	global_load_dword v108, v[10:11], off offset:256
	global_load_dword v107, v[12:13], off
	global_load_dword v105, v[12:13], off offset:256
	global_load_dword v103, v[14:15], off
	global_load_dword v101, v[14:15], off offset:256
	v_cndmask_b32_e64 v8, 27, 4, vcc
	v_or_b32_e32 v8, v1, v8
	v_cndmask_b32_e64 v10, 26, 5, vcc
	v_cndmask_b32_e64 v12, 25, 6, vcc
	v_cndmask_b32_e64 v14, 24, 7, vcc
	v_ashrrev_i32_e32 v9, 31, v8
	v_or_b32_e32 v10, v1, v10
	v_or_b32_e32 v12, v1, v12
	v_or_b32_e32 v14, v1, v14
	v_lshl_add_u64 v[60:61], v[8:9], 0, v[2:3]
	v_ashrrev_i32_e32 v11, 31, v10
	v_ashrrev_i32_e32 v13, 31, v12
	v_ashrrev_i32_e32 v15, 31, v14
	v_lshlrev_b64 v[8:9], 10, v[60:61]
	v_lshl_add_u64 v[58:59], v[10:11], 0, v[2:3]
	v_lshl_add_u64 v[56:57], v[12:13], 0, v[2:3]
	v_lshl_add_u64 v[54:55], v[14:15], 0, v[2:3]
	v_lshl_add_u64 v[8:9], v[80:81], 0, v[8:9]
	v_lshlrev_b64 v[10:11], 10, v[58:59]
	v_lshlrev_b64 v[12:13], 10, v[56:57]
	v_lshlrev_b64 v[14:15], 10, v[54:55]
	v_lshl_add_u64 v[8:9], v[8:9], 0, v[82:83]
	v_lshl_add_u64 v[10:11], v[80:81], 0, v[10:11]
	v_lshl_add_u64 v[12:13], v[80:81], 0, v[12:13]
	v_lshl_add_u64 v[14:15], v[80:81], 0, v[14:15]
	v_lshl_add_u64 v[10:11], v[10:11], 0, v[82:83]
	v_lshl_add_u64 v[12:13], v[12:13], 0, v[82:83]
	v_lshl_add_u64 v[14:15], v[14:15], 0, v[82:83]
	global_load_dword v106, v[8:9], off
	global_load_dword v104, v[8:9], off offset:256
	global_load_dword v102, v[10:11], off
	global_load_dword v100, v[10:11], off offset:256
	global_load_dword v99, v[12:13], off
	global_load_dword v97, v[12:13], off offset:256
	global_load_dword v95, v[14:15], off
	global_load_dword v93, v[14:15], off offset:256
	v_cndmask_b32_e64 v8, 23, 8, vcc
	v_or_b32_e32 v8, v1, v8
	v_cndmask_b32_e64 v10, 22, 9, vcc
	v_cndmask_b32_e64 v12, 21, 10, vcc
	v_cndmask_b32_e64 v14, 20, 11, vcc
	v_ashrrev_i32_e32 v9, 31, v8
	v_or_b32_e32 v10, v1, v10
	v_or_b32_e32 v12, v1, v12
	v_or_b32_e32 v14, v1, v14
	v_lshl_add_u64 v[52:53], v[8:9], 0, v[2:3]
	v_ashrrev_i32_e32 v11, 31, v10
	v_ashrrev_i32_e32 v13, 31, v12
	v_ashrrev_i32_e32 v15, 31, v14
	v_lshlrev_b64 v[8:9], 10, v[52:53]
; #define GAS __attribute__((address_space(1)))
; __device__ __forceinline__ void phase_carry(Frame& F, int l) {
;     ...
; #pragma unroll
;     for (int step = 0; step < 36; ++step) {
;         int inst; if (step < 4) inst = 256 + b * 4 + (d == 0 ? step : 3 - step); else inst = b * 32 + (d == 0 ? step - 4 : 35 - step);
;         const size_t row = (size_t)g * NINST + inst;
;         frv[step] = *(const GAS float*)(Fb + row * 256 + d * 128 + p); fiv[step] = *(const GAS float*)(Fb + row * 256 + d * 128 + 64 + p); }
	v_lshl_add_u64 v[50:51], v[10:11], 0, v[2:3]
	v_lshl_add_u64 v[48:49], v[12:13], 0, v[2:3]
	v_lshl_add_u64 v[46:47], v[14:15], 0, v[2:3]
	v_lshl_add_u64 v[8:9], v[80:81], 0, v[8:9]
	v_lshlrev_b64 v[10:11], 10, v[50:51]
	v_lshlrev_b64 v[12:13], 10, v[48:49]
	v_lshlrev_b64 v[14:15], 10, v[46:47]
	v_lshl_add_u64 v[8:9], v[8:9], 0, v[82:83]
	v_lshl_add_u64 v[10:11], v[80:81], 0, v[10:11]
	v_lshl_add_u64 v[12:13], v[80:81], 0, v[12:13]
	v_lshl_add_u64 v[14:15], v[80:81], 0, v[14:15]
	v_lshl_add_u64 v[10:11], v[10:11], 0, v[82:83]
	v_lshl_add_u64 v[12:13], v[12:13], 0, v[82:83]
	v_lshl_add_u64 v[14:15], v[14:15], 0, v[82:83]
	global_load_dword v98, v[8:9], off
	global_load_dword v96, v[8:9], off offset:256
	global_load_dword v94, v[10:11], off
	global_load_dword v92, v[10:11], off offset:256
	global_load_dword v91, v[12:13], off
	global_load_dword v89, v[12:13], off offset:256
	global_load_dword v87, v[14:15], off
	global_load_dword v85, v[14:15], off offset:256
	v_cndmask_b32_e64 v8, 19, 12, vcc
	v_or_b32_e32 v8, v1, v8
	v_cndmask_b32_e64 v10, 18, 13, vcc
	v_cndmask_b32_e64 v12, 17, 14, vcc
	v_or_b32_e32 v14, v17, v1
	v_ashrrev_i32_e32 v9, 31, v8
	v_or_b32_e32 v10, v1, v10
	v_or_b32_e32 v12, v1, v12
	v_add_u32_e32 v14, 15, v14
	v_lshl_add_u64 v[44:45], v[8:9], 0, v[2:3]
	v_ashrrev_i32_e32 v11, 31, v10
	v_ashrrev_i32_e32 v13, 31, v12
	v_ashrrev_i32_e32 v15, 31, v14
	v_lshlrev_b64 v[8:9], 10, v[44:45]
	v_lshl_add_u64 v[42:43], v[10:11], 0, v[2:3]
	v_lshl_add_u64 v[40:41], v[12:13], 0, v[2:3]
	v_lshl_add_u64 v[38:39], v[14:15], 0, v[2:3]
	v_lshl_add_u64 v[8:9], v[80:81], 0, v[8:9]
	v_lshlrev_b64 v[10:11], 10, v[42:43]
	v_lshlrev_b64 v[12:13], 10, v[40:41]
	v_lshlrev_b64 v[14:15], 10, v[38:39]
	v_lshl_add_u64 v[8:9], v[8:9], 0, v[82:83]
	v_lshl_add_u64 v[10:11], v[80:81], 0, v[10:11]
	v_lshl_add_u64 v[12:13], v[80:81], 0, v[12:13]
	v_lshl_add_u64 v[14:15], v[80:81], 0, v[14:15]
	v_lshl_add_u64 v[10:11], v[10:11], 0, v[82:83]
	v_lshl_add_u64 v[12:13], v[12:13], 0, v[82:83]
	v_lshl_add_u64 v[14:15], v[14:15], 0, v[82:83]
	global_load_dword v90, v[8:9], off
	global_load_dword v88, v[8:9], off offset:256
	global_load_dword v86, v[10:11], off
	global_load_dword v84, v[10:11], off offset:256
	global_load_dword v79, v[12:13], off
	global_load_dword v73, v[12:13], off offset:256
	global_load_dword v69, v[14:15], off
	global_load_dword v65, v[14:15], off offset:256
	v_sub_u32_e32 v8, v1, v17
	v_add_u32_e32 v8, 16, v8
	v_cndmask_b32_e64 v10, 14, 17, vcc
	v_cndmask_b32_e64 v12, 13, 18, vcc
	v_cndmask_b32_e64 v14, 12, 19, vcc
	v_ashrrev_i32_e32 v9, 31, v8
	v_or_b32_e32 v10, v1, v10
	v_or_b32_e32 v12, v1, v12
	v_or_b32_e32 v14, v1, v14
	v_lshl_add_u64 v[36:37], v[8:9], 0, v[2:3]
	v_ashrrev_i32_e32 v11, 31, v10
	v_ashrrev_i32_e32 v13, 31, v12
	v_ashrrev_i32_e32 v15, 31, v14
	v_lshlrev_b64 v[8:9], 10, v[36:37]
	v_lshl_add_u64 v[34:35], v[10:11], 0, v[2:3]
	v_lshl_add_u64 v[32:33], v[12:13], 0, v[2:3]
	v_lshl_add_u64 v[30:31], v[14:15], 0, v[2:3]
	v_lshl_add_u64 v[8:9], v[80:81], 0, v[8:9]
	v_lshlrev_b64 v[10:11], 10, v[34:35]
	v_lshlrev_b64 v[12:13], 10, v[32:33]
	v_lshlrev_b64 v[14:15], 10, v[30:31]
	v_lshl_add_u64 v[8:9], v[8:9], 0, v[82:83]
	v_lshl_add_u64 v[10:11], v[80:81], 0, v[10:11]
	v_lshl_add_u64 v[12:13], v[80:81], 0, v[12:13]
	v_lshl_add_u64 v[14:15], v[80:81], 0, v[14:15]
	v_lshl_add_u64 v[10:11], v[10:11], 0, v[82:83]
	v_lshl_add_u64 v[12:13], v[12:13], 0, v[82:83]
	v_lshl_add_u64 v[14:15], v[14:15], 0, v[82:83]
	global_load_dword v75, v[8:9], off
	global_load_dword v71, v[8:9], off offset:256
	global_load_dword v67, v[10:11], off
	global_load_dword v63, v[10:11], off offset:256
	global_load_dword v61, v[12:13], off
	global_load_dword v57, v[12:13], off offset:256
	global_load_dword v53, v[14:15], off
	global_load_dword v49, v[14:15], off offset:256
	v_cndmask_b32_e64 v8, 11, 20, vcc
	v_or_b32_e32 v8, v1, v8
	v_cndmask_b32_e64 v10, 10, 21, vcc
	v_cndmask_b32_e64 v12, 9, 22, vcc
	v_cndmask_b32_e64 v14, 8, 23, vcc
	v_ashrrev_i32_e32 v9, 31, v8
	v_or_b32_e32 v10, v1, v10
	v_or_b32_e32 v12, v1, v12
	v_or_b32_e32 v14, v1, v14
	v_lshl_add_u64 v[28:29], v[8:9], 0, v[2:3]
	v_ashrrev_i32_e32 v11, 31, v10
	v_ashrrev_i32_e32 v13, 31, v12
	v_ashrrev_i32_e32 v15, 31, v14
	v_lshlrev_b64 v[8:9], 10, v[28:29]
	v_lshl_add_u64 v[26:27], v[10:11], 0, v[2:3]
	v_lshl_add_u64 v[24:25], v[12:13], 0, v[2:3]
	v_lshl_add_u64 v[22:23], v[14:15], 0, v[2:3]
	v_lshl_add_u64 v[8:9], v[80:81], 0, v[8:9]
	v_lshlrev_b64 v[10:11], 10, v[26:27]
	v_lshlrev_b64 v[12:13], 10, v[24:25]
	v_lshlrev_b64 v[14:15], 10, v[22:23]
	v_lshl_add_u64 v[8:9], v[8:9], 0, v[82:83]
	v_lshl_add_u64 v[10:11], v[80:81], 0, v[10:11]
	v_lshl_add_u64 v[12:13], v[80:81], 0, v[12:13]
	v_lshl_add_u64 v[14:15], v[80:81], 0, v[14:15]
	v_lshl_add_u64 v[10:11], v[10:11], 0, v[82:83]
	v_lshl_add_u64 v[12:13], v[12:13], 0, v[82:83]
	v_lshl_add_u64 v[14:15], v[14:15], 0, v[82:83]
	global_load_dword v59, v[8:9], off
	global_load_dword v55, v[8:9], off offset:256
	global_load_dword v51, v[10:11], off
	global_load_dword v47, v[10:11], off offset:256
	global_load_dword v45, v[12:13], off
	global_load_dword v41, v[12:13], off offset:256
	global_load_dword v37, v[14:15], off
	global_load_dword v33, v[14:15], off offset:256
	v_cndmask_b32_e64 v8, 7, 24, vcc
	v_or_b32_e32 v8, v1, v8
	v_cndmask_b32_e64 v10, 6, 25, vcc
	v_cndmask_b32_e64 v12, 5, 26, vcc
	v_cndmask_b32_e64 v14, 4, 27, vcc
	v_ashrrev_i32_e32 v9, 31, v8
	v_or_b32_e32 v10, v1, v10
	v_or_b32_e32 v12, v1, v12
	v_or_b32_e32 v14, v1, v14
	v_lshl_add_u64 v[20:21], v[8:9], 0, v[2:3]
	v_ashrrev_i32_e32 v11, 31, v10
	v_ashrrev_i32_e32 v13, 31, v12
	v_ashrrev_i32_e32 v15, 31, v14
; #define GAS __attribute__((address_space(1)))
; __device__ __forceinline__ void phase_carry(Frame& F, int l) {
;     ...
; #pragma unroll
;     for (int step = 0; step < 36; ++step) {
;         int inst; if (step < 4) inst = 256 + b * 4 + (d == 0 ? step : 3 - step); else inst = b * 32 + (d == 0 ? step - 4 : 35 - step);
;         const size_t row = (size_t)g * NINST + inst;
;         frv[step] = *(const GAS float*)(Fb + row * 256 + d * 128 + p); fiv[step] = *(const GAS float*)(Fb + row * 256 + d * 128 + 64 + p); }
; #pragma unroll
;     for (int step = 0; step < 36; ++step) {
;         int inst; if (step < 4) inst = 256 + b * 4 + (d == 0 ? step : 3 - step); else inst = b * 32 + (d == 0 ? step - 4 : 35 - step);
;         const size_t row = (size_t)g * NINST + inst;
;         a8[row * KS2 + 1024 + d * 128 + p] = (unsigned char)(pk4_fp8(hr * S5_SH, 0.f, 0.f, 0.f) & 0xffu); a8[row * KS2 + 1024 + d * 128 + 64 + p] = (unsigned char)(pk4_fp8(hi * S5_SH, 0.f, 0.f, 0.f) & 0xffu);
;         const float nr = lt.x * hr - lt.y * hi + frv[step]; hi = lt.x * hi + lt.y * hr + fiv[step]; hr = nr; }
	v_lshlrev_b32_e32 v76, 7, v17
	v_lshlrev_b64 v[8:9], 10, v[20:21]
	v_lshl_add_u64 v[18:19], v[10:11], 0, v[2:3]
	v_lshl_add_u64 v[16:17], v[12:13], 0, v[2:3]
	v_lshl_add_u64 v[14:15], v[14:15], 0, v[2:3]
	v_lshl_add_u64 v[8:9], v[80:81], 0, v[8:9]
	v_lshlrev_b64 v[10:11], 10, v[18:19]
	v_lshlrev_b64 v[12:13], 10, v[16:17]
	v_lshlrev_b64 v[116:117], 10, v[14:15]
	v_lshl_add_u64 v[8:9], v[8:9], 0, v[82:83]
	v_lshl_add_u64 v[10:11], v[80:81], 0, v[10:11]
	v_lshl_add_u64 v[12:13], v[80:81], 0, v[12:13]
	v_lshl_add_u64 v[116:117], v[80:81], 0, v[116:117]
	v_lshl_add_u64 v[10:11], v[10:11], 0, v[82:83]
	v_lshl_add_u64 v[12:13], v[12:13], 0, v[82:83]
	v_lshl_add_u64 v[116:117], v[116:117], 0, v[82:83]
	global_load_dword v43, v[8:9], off
	global_load_dword v39, v[8:9], off offset:256
	global_load_dword v35, v[10:11], off
	global_load_dword v31, v[10:11], off offset:256
	global_load_dword v29, v[12:13], off
	global_load_dword v27, v[12:13], off offset:256
	global_load_dword v21, v[116:117], off
	global_load_dword v19, v[116:117], off offset:256
	v_cndmask_b32_e64 v8, 3, 28, vcc
	v_or_b32_e32 v8, v1, v8
	v_ashrrev_i32_e32 v9, 31, v8
	v_lshl_add_u64 v[12:13], v[8:9], 0, v[2:3]
	v_lshlrev_b64 v[8:9], 10, v[12:13]
	v_lshl_add_u64 v[8:9], v[80:81], 0, v[8:9]
	v_lshl_add_u64 v[116:117], v[8:9], 0, v[82:83]
	v_cndmask_b32_e64 v8, 2, 29, vcc
	v_or_b32_e32 v8, v1, v8
	v_ashrrev_i32_e32 v9, 31, v8
	v_lshl_add_u64 v[10:11], v[8:9], 0, v[2:3]
	v_lshlrev_b64 v[8:9], 10, v[10:11]
	v_lshl_add_u64 v[8:9], v[80:81], 0, v[8:9]
	v_lshl_add_u64 v[118:119], v[8:9], 0, v[82:83]
	v_cndmask_b32_e64 v8, 1, 30, vcc
	v_or_b32_e32 v8, v1, v8
	v_ashrrev_i32_e32 v9, 31, v8
	v_lshl_add_u64 v[8:9], v[8:9], 0, v[2:3]
	v_lshlrev_b64 v[120:121], 10, v[8:9]
	v_lshl_add_u64 v[80:81], v[80:81], 0, v[120:121]
	v_lshl_add_u64 v[80:81], v[80:81], 0, v[82:83]
	global_load_dword v25, v[116:117], off
	global_load_dword v23, v[116:117], off offset:256
	global_load_dword v17, v[118:119], off
	global_load_dword v15, v[118:119], off offset:256
	global_load_dword v11, v[80:81], off
	global_load_dword v9, v[80:81], off offset:256
	v_mov_b32_e32 v80, v3
	v_cvt_pk_fp8_f32 v80, 0, 0
	v_mov_b32_e32 v77, v3
	v_mov_b32_e32 v7, v3
	v_lshl_add_u64 v[76:77], s[2:3], 0, v[76:77]
	v_cvt_pk_fp8_f32 v80, 0, 0 op_sel:[0,0,1]
	v_lshl_add_u64 v[6:7], v[76:77], 0, v[6:7]
	s_mov_b64 s[0:1], 0x6ab00400
	v_mul_hi_i32_i24_e32 v77, 0x500, v78
	v_mul_i32_i24_e32 v76, 0x500, v78
	s_waitcnt vmcnt(0) lgkmcnt(0)
	v_mul_f32_e32 v78, 0, v5
	v_lshl_add_u64 v[6:7], v[6:7], 0, s[0:1]
	v_fma_f32 v13, v4, 0, -v78
	v_fmac_f32_e32 v78, 0, v4
	v_lshl_add_u64 v[76:77], v[6:7], 0, v[76:77]
	v_add_f32_e32 v78, v122, v78
	global_store_byte v[76:77], v80, off sc1
	v_add_f32_e32 v81, v115, v13
	s_mov_b32 s1, 0xc3e00000
	v_mov_b32_e32 v13, 0x43e00000
	global_store_byte v[76:77], v80, off offset:64 sc1
	v_mul_f32_e32 v76, 0x43000000, v78
	v_med3_f32 v76, v76, s1, v13
	v_mov_b32_e32 v80, v3
	v_cvt_pk_fp8_f32 v80, v76, 0
	v_mul_hi_i32_i24_e32 v77, 0x500, v74
	v_mul_i32_i24_e32 v76, 0x500, v74
	v_mul_f32_e32 v74, v5, v78
	v_mul_f32_e32 v82, 0x43000000, v81
	v_fma_f32 v74, v4, v81, -v74
	v_mul_f32_e32 v81, v5, v81
	v_med3_f32 v82, v82, s1, v13
	v_add_f32_e32 v74, v123, v74
	v_fmac_f32_e32 v81, v4, v78
	v_cvt_pk_fp8_f32 v83, v82, 0
	v_add_f32_e32 v78, v124, v81
	v_mul_f32_e32 v81, 0x43000000, v74
	v_med3_f32 v81, v81, s1, v13
	v_mov_b32_e32 v82, v3
	v_cvt_pk_fp8_f32 v82, v81, 0
	v_mul_f32_e32 v81, 0x43000000, v78
	v_med3_f32 v81, v81, s1, v13
	v_mov_b32_e32 v115, v3
	v_cvt_pk_fp8_f32 v83, 0, 0 op_sel:[0,0,1]
	v_cvt_pk_fp8_f32 v115, v81, 0
	v_cvt_pk_fp8_f32 v80, 0, 0 op_sel:[0,0,1]
	s_movk_i32 s0, 0x500
	v_lshl_add_u64 v[76:77], v[6:7], 0, v[76:77]
	v_cvt_pk_fp8_f32 v82, 0, 0 op_sel:[0,0,1]
	global_store_byte v[76:77], v83, off sc1
	global_store_byte v[76:77], v80, off offset:64 sc1
	v_cvt_pk_fp8_f32 v115, 0, 0 op_sel:[0,0,1]
	v_mad_i64_i32 v[76:77], s[6:7], v72, s0, v[6:7]
	v_mul_f32_e32 v72, v5, v78
	v_fma_f32 v72, v4, v74, -v72
	v_add_f32_e32 v72, v125, v72
	v_mul_f32_e32 v74, v5, v74
	global_store_byte v[76:77], v82, off sc1
	global_store_byte v[76:77], v115, off offset:64 sc1
	v_mul_f32_e32 v76, 0x43000000, v72
	v_fmac_f32_e32 v74, v4, v78
	v_med3_f32 v76, v76, s1, v13
	v_mov_b32_e32 v80, v3
	v_add_f32_e32 v74, v113, v74
	v_cvt_pk_fp8_f32 v80, v76, 0
	v_mul_f32_e32 v76, 0x43000000, v74
	v_med3_f32 v76, v76, s1, v13
	v_mov_b32_e32 v78, v3
	v_cvt_pk_fp8_f32 v78, v76, 0
	v_mul_hi_i32_i24_e32 v77, 0x500, v70
	v_mul_i32_i24_e32 v76, 0x500, v70
	v_mul_f32_e32 v70, v5, v74
	v_fma_f32 v70, v4, v72, -v70
	v_add_f32_e32 v70, v111, v70
	v_mul_f32_e32 v72, v5, v72
	v_fmac_f32_e32 v72, v4, v74
	v_mul_f32_e32 v74, 0x43000000, v70
	v_cvt_pk_fp8_f32 v80, 0, 0 op_sel:[0,0,1]
	v_add_f32_e32 v72, v109, v72
	v_med3_f32 v74, v74, s1, v13
	v_mov_b32_e32 v81, v3
	v_cvt_pk_fp8_f32 v78, 0, 0 op_sel:[0,0,1]
	v_cvt_pk_fp8_f32 v81, v74, 0
	v_mul_f32_e32 v74, 0x43000000, v72
	v_med3_f32 v74, v74, s1, v13
	v_mov_b32_e32 v82, v3
	v_lshl_add_u64 v[76:77], v[6:7], 0, v[76:77]
	v_cvt_pk_fp8_f32 v82, v74, 0
	global_store_byte v[76:77], v80, off sc1
	global_store_byte v[76:77], v78, off offset:64 sc1
	v_mad_i64_i32 v[76:77], s[6:7], v68, s0, v[6:7]
	v_mul_f32_e32 v68, v5, v72
	v_fma_f32 v68, v4, v70, -v68
	v_cvt_pk_fp8_f32 v81, 0, 0 op_sel:[0,0,1]
	v_add_f32_e32 v68, v114, v68
	v_mul_f32_e32 v70, v5, v70
	v_cvt_pk_fp8_f32 v82, 0, 0 op_sel:[0,0,1]
	v_fmac_f32_e32 v70, v4, v72
	v_mul_f32_e32 v72, 0x43000000, v68
	v_add_f32_e32 v70, v112, v70
	v_med3_f32 v72, v72, s1, v13
	v_mov_b32_e32 v74, v3
	v_cvt_pk_fp8_f32 v74, v72, 0
	v_mul_f32_e32 v72, 0x43000000, v70
; __device__ __forceinline__ void phase_carry(Frame& F, int l) {
;     ...
; #pragma unroll
;     for (int step = 0; step < 36; ++step) {
;         int inst; if (step < 4) inst = 256 + b * 4 + (d == 0 ? step : 3 - step); else inst = b * 32 + (d == 0 ? step - 4 : 35 - step);
;         const size_t row = (size_t)g * NINST + inst;
;         a8[row * KS2 + 1024 + d * 128 + p] = (unsigned char)(pk4_fp8(hr * S5_SH, 0.f, 0.f, 0.f) & 0xffu); a8[row * KS2 + 1024 + d * 128 + 64 + p] = (unsigned char)(pk4_fp8(hi * S5_SH, 0.f, 0.f, 0.f) & 0xffu);
;         const float nr = lt.x * hr - lt.y * hi + frv[step]; hi = lt.x * hi + lt.y * hr + fiv[step]; hr = nr; }
	global_store_byte v[76:77], v81, off sc1
	global_store_byte v[76:77], v82, off offset:64 sc1
	v_med3_f32 v72, v72, s1, v13
	v_mov_b32_e32 v78, v3
	v_mad_i64_i32 v[76:77], s[6:7], v66, s0, v[6:7]
	v_mul_f32_e32 v66, v5, v70
	v_cvt_pk_fp8_f32 v78, v72, 0
	v_fma_f32 v66, v4, v68, -v66
	v_add_f32_e32 v66, v110, v66
	v_mul_f32_e32 v68, v5, v68
	v_fmac_f32_e32 v68, v4, v70
	v_mul_f32_e32 v70, 0x43000000, v66
	v_cvt_pk_fp8_f32 v74, 0, 0 op_sel:[0,0,1]
	v_add_f32_e32 v68, v108, v68
	v_med3_f32 v70, v70, s1, v13
	v_mov_b32_e32 v72, v3
	v_cvt_pk_fp8_f32 v78, 0, 0 op_sel:[0,0,1]
	v_cvt_pk_fp8_f32 v72, v70, 0
	v_mul_f32_e32 v70, 0x43000000, v68
	v_med3_f32 v70, v70, s1, v13
	v_mov_b32_e32 v80, v3
	v_cvt_pk_fp8_f32 v80, v70, 0
	global_store_byte v[76:77], v74, off sc1
	global_store_byte v[76:77], v78, off offset:64 sc1
	v_mad_i64_i32 v[76:77], s[6:7], v64, s0, v[6:7]
	v_mul_f32_e32 v64, v5, v68
	v_fma_f32 v64, v4, v66, -v64
	v_cvt_pk_fp8_f32 v72, 0, 0 op_sel:[0,0,1]
	v_add_f32_e32 v64, v107, v64
	v_mul_f32_e32 v66, v5, v66
	v_cvt_pk_fp8_f32 v80, 0, 0 op_sel:[0,0,1]
	v_fmac_f32_e32 v66, v4, v68
	v_mul_f32_e32 v68, 0x43000000, v64
	v_add_f32_e32 v66, v105, v66
	v_med3_f32 v68, v68, s1, v13
	v_mov_b32_e32 v70, v3
	v_cvt_pk_fp8_f32 v70, v68, 0
	v_mul_f32_e32 v68, 0x43000000, v66
	global_store_byte v[76:77], v72, off sc1
	global_store_byte v[76:77], v80, off offset:64 sc1
	v_med3_f32 v68, v68, s1, v13
	v_mov_b32_e32 v72, v3
	v_mad_i64_i32 v[76:77], s[6:7], v62, s0, v[6:7]
	v_mul_f32_e32 v62, v5, v66
	v_cvt_pk_fp8_f32 v72, v68, 0
	v_fma_f32 v62, v4, v64, -v62
	v_add_f32_e32 v62, v103, v62
	v_mul_f32_e32 v64, v5, v64
	v_fmac_f32_e32 v64, v4, v66
	v_mul_f32_e32 v66, 0x43000000, v62
	v_cvt_pk_fp8_f32 v70, 0, 0 op_sel:[0,0,1]
	v_add_f32_e32 v64, v101, v64
	v_med3_f32 v66, v66, s1, v13
	v_mov_b32_e32 v68, v3
	v_cvt_pk_fp8_f32 v72, 0, 0 op_sel:[0,0,1]
	v_cvt_pk_fp8_f32 v68, v66, 0
	v_mul_f32_e32 v66, 0x43000000, v64
	v_med3_f32 v66, v66, s1, v13
	v_mov_b32_e32 v74, v3
	v_cvt_pk_fp8_f32 v74, v66, 0
	global_store_byte v[76:77], v70, off sc1
	global_store_byte v[76:77], v72, off offset:64 sc1
	v_mad_i64_i32 v[76:77], s[6:7], v60, s0, v[6:7]
	v_mul_f32_e32 v60, v5, v64
	v_fma_f32 v60, v4, v62, -v60
	v_cvt_pk_fp8_f32 v68, 0, 0 op_sel:[0,0,1]
	v_add_f32_e32 v60, v106, v60
	v_mul_f32_e32 v62, v5, v62
	v_cvt_pk_fp8_f32 v74, 0, 0 op_sel:[0,0,1]
	v_fmac_f32_e32 v62, v4, v64
	v_mul_f32_e32 v64, 0x43000000, v60
	v_add_f32_e32 v62, v104, v62
	v_med3_f32 v64, v64, s1, v13
	v_mov_b32_e32 v66, v3
	v_cvt_pk_fp8_f32 v66, v64, 0
	v_mul_f32_e32 v64, 0x43000000, v62
	global_store_byte v[76:77], v68, off sc1
	global_store_byte v[76:77], v74, off offset:64 sc1
	v_med3_f32 v64, v64, s1, v13
	v_mov_b32_e32 v68, v3
	v_mad_i64_i32 v[76:77], s[6:7], v58, s0, v[6:7]
	v_mul_f32_e32 v58, v5, v62
	v_cvt_pk_fp8_f32 v68, v64, 0
	v_fma_f32 v58, v4, v60, -v58
	v_add_f32_e32 v58, v102, v58
	v_mul_f32_e32 v60, v5, v60
	v_fmac_f32_e32 v60, v4, v62
	v_mul_f32_e32 v62, 0x43000000, v58
	v_cvt_pk_fp8_f32 v66, 0, 0 op_sel:[0,0,1]
	v_add_f32_e32 v60, v100, v60
	v_med3_f32 v62, v62, s1, v13
	v_mov_b32_e32 v64, v3
	v_cvt_pk_fp8_f32 v68, 0, 0 op_sel:[0,0,1]
	v_cvt_pk_fp8_f32 v64, v62, 0
	v_mul_f32_e32 v62, 0x43000000, v60
	v_med3_f32 v62, v62, s1, v13
	v_mov_b32_e32 v70, v3
	v_cvt_pk_fp8_f32 v70, v62, 0
	global_store_byte v[76:77], v66, off sc1
	global_store_byte v[76:77], v68, off offset:64 sc1
	v_mad_i64_i32 v[76:77], s[6:7], v56, s0, v[6:7]
	v_mul_f32_e32 v56, v5, v60
	v_fma_f32 v56, v4, v58, -v56
	v_cvt_pk_fp8_f32 v64, 0, 0 op_sel:[0,0,1]
	v_add_f32_e32 v56, v99, v56
	v_mul_f32_e32 v58, v5, v58
	v_cvt_pk_fp8_f32 v70, 0, 0 op_sel:[0,0,1]
	v_fmac_f32_e32 v58, v4, v60
	v_mul_f32_e32 v60, 0x43000000, v56
	v_add_f32_e32 v58, v97, v58
	v_med3_f32 v60, v60, s1, v13
	v_mov_b32_e32 v62, v3
	v_cvt_pk_fp8_f32 v62, v60, 0
	v_mul_f32_e32 v60, 0x43000000, v58
	global_store_byte v[76:77], v64, off sc1
	global_store_byte v[76:77], v70, off offset:64 sc1
	v_med3_f32 v60, v60, s1, v13
	v_mov_b32_e32 v64, v3
	v_mad_i64_i32 v[76:77], s[6:7], v54, s0, v[6:7]
	v_mul_f32_e32 v54, v5, v58
	v_cvt_pk_fp8_f32 v64, v60, 0
	v_fma_f32 v54, v4, v56, -v54
	v_add_f32_e32 v54, v95, v54
	v_mul_f32_e32 v56, v5, v56
	v_fmac_f32_e32 v56, v4, v58
	v_mul_f32_e32 v58, 0x43000000, v54
	v_cvt_pk_fp8_f32 v62, 0, 0 op_sel:[0,0,1]
	v_add_f32_e32 v56, v93, v56
	v_med3_f32 v58, v58, s1, v13
	v_mov_b32_e32 v60, v3
	v_cvt_pk_fp8_f32 v64, 0, 0 op_sel:[0,0,1]
	v_cvt_pk_fp8_f32 v60, v58, 0
	v_mul_f32_e32 v58, 0x43000000, v56
	v_med3_f32 v58, v58, s1, v13
	v_mov_b32_e32 v66, v3
	v_cvt_pk_fp8_f32 v66, v58, 0
	global_store_byte v[76:77], v62, off sc1
	global_store_byte v[76:77], v64, off offset:64 sc1
	v_mad_i64_i32 v[76:77], s[6:7], v52, s0, v[6:7]
	v_mul_f32_e32 v52, v5, v56
	v_fma_f32 v52, v4, v54, -v52
	v_cvt_pk_fp8_f32 v60, 0, 0 op_sel:[0,0,1]
	v_add_f32_e32 v52, v98, v52
	v_mul_f32_e32 v54, v5, v54
	v_cvt_pk_fp8_f32 v66, 0, 0 op_sel:[0,0,1]
	v_fmac_f32_e32 v54, v4, v56
	v_mul_f32_e32 v56, 0x43000000, v52
	v_add_f32_e32 v54, v96, v54
	v_med3_f32 v56, v56, s1, v13
	v_mov_b32_e32 v58, v3
	v_cvt_pk_fp8_f32 v58, v56, 0
	v_mul_f32_e32 v56, 0x43000000, v54
	global_store_byte v[76:77], v60, off sc1
	global_store_byte v[76:77], v66, off offset:64 sc1
	v_med3_f32 v56, v56, s1, v13
	v_mov_b32_e32 v60, v3
	v_mad_i64_i32 v[76:77], s[6:7], v50, s0, v[6:7]
	v_mul_f32_e32 v50, v5, v54
	v_cvt_pk_fp8_f32 v60, v56, 0
	v_fma_f32 v50, v4, v52, -v50
	v_add_f32_e32 v50, v94, v50
	v_mul_f32_e32 v52, v5, v52
	v_fmac_f32_e32 v52, v4, v54
	v_mul_f32_e32 v54, 0x43000000, v50
	v_cvt_pk_fp8_f32 v58, 0, 0 op_sel:[0,0,1]
	v_add_f32_e32 v52, v92, v52
	v_med3_f32 v54, v54, s1, v13
; __device__ __forceinline__ void phase_carry(Frame& F, int l) {
;     ...
; #pragma unroll
;     for (int step = 0; step < 36; ++step) {
;         int inst; if (step < 4) inst = 256 + b * 4 + (d == 0 ? step : 3 - step); else inst = b * 32 + (d == 0 ? step - 4 : 35 - step);
;         const size_t row = (size_t)g * NINST + inst;
;         a8[row * KS2 + 1024 + d * 128 + p] = (unsigned char)(pk4_fp8(hr * S5_SH, 0.f, 0.f, 0.f) & 0xffu); a8[row * KS2 + 1024 + d * 128 + 64 + p] = (unsigned char)(pk4_fp8(hi * S5_SH, 0.f, 0.f, 0.f) & 0xffu);
;         const float nr = lt.x * hr - lt.y * hi + frv[step]; hi = lt.x * hi + lt.y * hr + fiv[step]; hr = nr; }
	v_mov_b32_e32 v56, v3
	v_cvt_pk_fp8_f32 v60, 0, 0 op_sel:[0,0,1]
	v_cvt_pk_fp8_f32 v56, v54, 0
	v_mul_f32_e32 v54, 0x43000000, v52
	v_med3_f32 v54, v54, s1, v13
	v_mov_b32_e32 v62, v3
	v_cvt_pk_fp8_f32 v62, v54, 0
	global_store_byte v[76:77], v58, off sc1
	global_store_byte v[76:77], v60, off offset:64 sc1
	v_mad_i64_i32 v[76:77], s[6:7], v48, s0, v[6:7]
	v_mul_f32_e32 v48, v5, v52
	v_fma_f32 v48, v4, v50, -v48
	v_cvt_pk_fp8_f32 v56, 0, 0 op_sel:[0,0,1]
	v_add_f32_e32 v48, v91, v48
	v_mul_f32_e32 v50, v5, v50
	v_cvt_pk_fp8_f32 v62, 0, 0 op_sel:[0,0,1]
	v_fmac_f32_e32 v50, v4, v52
	v_mul_f32_e32 v52, 0x43000000, v48
	v_add_f32_e32 v50, v89, v50
	v_med3_f32 v52, v52, s1, v13
	v_mov_b32_e32 v54, v3
	v_cvt_pk_fp8_f32 v54, v52, 0
	v_mul_f32_e32 v52, 0x43000000, v50
	global_store_byte v[76:77], v56, off sc1
	global_store_byte v[76:77], v62, off offset:64 sc1
	v_med3_f32 v52, v52, s1, v13
	v_mov_b32_e32 v56, v3
	v_mad_i64_i32 v[76:77], s[6:7], v46, s0, v[6:7]
	v_mul_f32_e32 v46, v5, v50
	v_cvt_pk_fp8_f32 v56, v52, 0
	v_fma_f32 v46, v4, v48, -v46
	v_add_f32_e32 v46, v87, v46
	v_mul_f32_e32 v48, v5, v48
	v_fmac_f32_e32 v48, v4, v50
	v_mul_f32_e32 v50, 0x43000000, v46
	v_cvt_pk_fp8_f32 v54, 0, 0 op_sel:[0,0,1]
	v_add_f32_e32 v48, v85, v48
	v_med3_f32 v50, v50, s1, v13
	v_mov_b32_e32 v52, v3
	v_cvt_pk_fp8_f32 v56, 0, 0 op_sel:[0,0,1]
	v_cvt_pk_fp8_f32 v52, v50, 0
	v_mul_f32_e32 v50, 0x43000000, v48
	v_med3_f32 v50, v50, s1, v13
	v_mov_b32_e32 v58, v3
	v_cvt_pk_fp8_f32 v58, v50, 0
	global_store_byte v[76:77], v54, off sc1
	global_store_byte v[76:77], v56, off offset:64 sc1
	v_mad_i64_i32 v[76:77], s[6:7], v44, s0, v[6:7]
	v_mul_f32_e32 v44, v5, v48
	v_fma_f32 v44, v4, v46, -v44
	v_cvt_pk_fp8_f32 v52, 0, 0 op_sel:[0,0,1]
	v_add_f32_e32 v44, v90, v44
	v_mul_f32_e32 v46, v5, v46
	v_cvt_pk_fp8_f32 v58, 0, 0 op_sel:[0,0,1]
	v_fmac_f32_e32 v46, v4, v48
	v_mul_f32_e32 v48, 0x43000000, v44
	v_add_f32_e32 v46, v88, v46
	v_med3_f32 v48, v48, s1, v13
	v_mov_b32_e32 v50, v3
	v_cvt_pk_fp8_f32 v50, v48, 0
	v_mul_f32_e32 v48, 0x43000000, v46
	global_store_byte v[76:77], v52, off sc1
	global_store_byte v[76:77], v58, off offset:64 sc1
	v_med3_f32 v48, v48, s1, v13
	v_mov_b32_e32 v52, v3
	v_cvt_pk_fp8_f32 v52, v48, 0
	v_mad_i64_i32 v[76:77], s[6:7], v42, s0, v[6:7]
	v_mul_f32_e32 v42, v5, v46
	v_fma_f32 v42, v4, v44, -v42
	v_add_f32_e32 v42, v86, v42
	v_mul_f32_e32 v44, v5, v44
	v_cvt_pk_fp8_f32 v50, 0, 0 op_sel:[0,0,1]
	v_fmac_f32_e32 v44, v4, v46
	v_mul_f32_e32 v46, 0x43000000, v42
	v_cvt_pk_fp8_f32 v52, 0, 0 op_sel:[0,0,1]
	v_add_f32_e32 v44, v84, v44
	v_med3_f32 v46, v46, s1, v13
	v_mov_b32_e32 v48, v3
	v_cvt_pk_fp8_f32 v48, v46, 0
	v_mul_f32_e32 v46, 0x43000000, v44
	v_med3_f32 v46, v46, s1, v13
	v_mov_b32_e32 v54, v3
	v_cvt_pk_fp8_f32 v54, v46, 0
	global_store_byte v[76:77], v50, off sc1
	global_store_byte v[76:77], v52, off offset:64 sc1
	v_mad_i64_i32 v[76:77], s[6:7], v40, s0, v[6:7]
	v_mul_f32_e32 v40, v5, v44
	v_fma_f32 v40, v4, v42, -v40
	v_mul_f32_e32 v42, v5, v42
	v_fmac_f32_e32 v42, v4, v44
	v_cvt_pk_fp8_f32 v48, 0, 0 op_sel:[0,0,1]
	v_add_f32_e32 v40, v79, v40
	v_add_f32_e32 v42, v73, v42
	v_cvt_pk_fp8_f32 v54, 0, 0 op_sel:[0,0,1]
	v_mul_f32_e32 v44, 0x43000000, v40
	v_mad_i64_i32 v[72:73], s[6:7], v38, s0, v[6:7]
	v_mul_f32_e32 v38, v5, v42
	v_med3_f32 v44, v44, s1, v13
	v_mov_b32_e32 v46, v3
	v_fma_f32 v38, v4, v40, -v38
	v_cvt_pk_fp8_f32 v46, v44, 0
	v_mul_f32_e32 v44, 0x43000000, v42
	v_add_f32_e32 v38, v69, v38
	v_mul_f32_e32 v40, v5, v40
	global_store_byte v[76:77], v48, off sc1
	global_store_byte v[76:77], v54, off offset:64 sc1
	v_med3_f32 v44, v44, s1, v13
	v_mov_b32_e32 v48, v3
	v_fmac_f32_e32 v40, v4, v42
	v_mul_f32_e32 v42, 0x43000000, v38
	v_cvt_pk_fp8_f32 v48, v44, 0
	v_add_f32_e32 v40, v65, v40
	v_med3_f32 v42, v42, s1, v13
	v_mov_b32_e32 v44, v3
	v_cvt_pk_fp8_f32 v44, v42, 0
	v_mul_f32_e32 v42, 0x43000000, v40
	v_med3_f32 v42, v42, s1, v13
	v_mov_b32_e32 v50, v3
	v_cvt_pk_fp8_f32 v50, v42, 0
	v_cvt_pk_fp8_f32 v46, 0, 0 op_sel:[0,0,1]
	v_cvt_pk_fp8_f32 v44, 0, 0 op_sel:[0,0,1]
	v_mad_i64_i32 v[64:65], s[6:7], v36, s0, v[6:7]
	v_mul_f32_e32 v36, v5, v40
	v_cvt_pk_fp8_f32 v48, 0, 0 op_sel:[0,0,1]
	v_cvt_pk_fp8_f32 v50, 0, 0 op_sel:[0,0,1]
	v_fma_f32 v36, v4, v38, -v36
	v_mul_f32_e32 v38, v5, v38
	v_fmac_f32_e32 v38, v4, v40
	v_add_f32_e32 v36, v75, v36
	v_add_f32_e32 v38, v71, v38
	global_store_byte v[72:73], v46, off sc1
	global_store_byte v[72:73], v48, off offset:64 sc1
	global_store_byte v[64:65], v44, off sc1
	global_store_byte v[64:65], v50, off offset:64 sc1
	v_mul_f32_e32 v40, 0x43000000, v36
	v_mad_i64_i32 v[64:65], s[6:7], v34, s0, v[6:7]
	v_mul_f32_e32 v34, v5, v38
	v_med3_f32 v40, v40, s1, v13
	v_mov_b32_e32 v42, v3
	v_fma_f32 v34, v4, v36, -v34
	v_cvt_pk_fp8_f32 v42, v40, 0
	v_mul_f32_e32 v40, 0x43000000, v38
	v_add_f32_e32 v34, v67, v34
	v_mul_f32_e32 v36, v5, v36
	v_med3_f32 v40, v40, s1, v13
	v_mov_b32_e32 v44, v3
	v_fmac_f32_e32 v36, v4, v38
	v_mul_f32_e32 v38, 0x43000000, v34
	v_cvt_pk_fp8_f32 v44, v40, 0
	v_add_f32_e32 v36, v63, v36
	v_med3_f32 v38, v38, s1, v13
	v_mov_b32_e32 v40, v3
	v_cvt_pk_fp8_f32 v40, v38, 0
	v_mul_f32_e32 v38, 0x43000000, v36
	v_med3_f32 v38, v38, s1, v13
	v_mov_b32_e32 v46, v3
	v_cvt_pk_fp8_f32 v46, v38, 0
	v_mad_i64_i32 v[62:63], s[6:7], v32, s0, v[6:7]
	v_mul_f32_e32 v32, v5, v36
	v_fma_f32 v32, v4, v34, -v32
	v_mul_f32_e32 v34, v5, v34
	v_fmac_f32_e32 v34, v4, v36
	v_cvt_pk_fp8_f32 v42, 0, 0 op_sel:[0,0,1]
	v_cvt_pk_fp8_f32 v40, 0, 0 op_sel:[0,0,1]
	v_add_f32_e32 v32, v61, v32
	v_add_f32_e32 v34, v57, v34
	v_cvt_pk_fp8_f32 v44, 0, 0 op_sel:[0,0,1]
	v_cvt_pk_fp8_f32 v46, 0, 0 op_sel:[0,0,1]
; __device__ __forceinline__ void phase_carry(Frame& F, int l) {
;     ...
; #pragma unroll
;     for (int step = 0; step < 36; ++step) {
;         int inst; if (step < 4) inst = 256 + b * 4 + (d == 0 ? step : 3 - step); else inst = b * 32 + (d == 0 ? step - 4 : 35 - step);
;         const size_t row = (size_t)g * NINST + inst;
;         a8[row * KS2 + 1024 + d * 128 + p] = (unsigned char)(pk4_fp8(hr * S5_SH, 0.f, 0.f, 0.f) & 0xffu); a8[row * KS2 + 1024 + d * 128 + 64 + p] = (unsigned char)(pk4_fp8(hi * S5_SH, 0.f, 0.f, 0.f) & 0xffu);
;         const float nr = lt.x * hr - lt.y * hi + frv[step]; hi = lt.x * hi + lt.y * hr + fiv[step]; hr = nr; }
	v_mul_f32_e32 v36, 0x43000000, v32
	v_mad_i64_i32 v[56:57], s[6:7], v30, s0, v[6:7]
	v_mul_f32_e32 v30, v5, v34
	v_med3_f32 v36, v36, s1, v13
	v_mov_b32_e32 v38, v3
	v_fma_f32 v30, v4, v32, -v30
	v_cvt_pk_fp8_f32 v38, v36, 0
	v_mul_f32_e32 v36, 0x43000000, v34
	v_add_f32_e32 v30, v53, v30
	v_mul_f32_e32 v32, v5, v32
	global_store_byte v[64:65], v42, off sc1
	global_store_byte v[64:65], v44, off offset:64 sc1
	global_store_byte v[62:63], v40, off sc1
	global_store_byte v[62:63], v46, off offset:64 sc1
	v_med3_f32 v36, v36, s1, v13
	v_mov_b32_e32 v40, v3
	v_fmac_f32_e32 v32, v4, v34
	v_mul_f32_e32 v34, 0x43000000, v30
	v_cvt_pk_fp8_f32 v40, v36, 0
	v_add_f32_e32 v32, v49, v32
	v_med3_f32 v34, v34, s1, v13
	v_mov_b32_e32 v36, v3
	v_cvt_pk_fp8_f32 v36, v34, 0
	v_mul_f32_e32 v34, 0x43000000, v32
	v_med3_f32 v34, v34, s1, v13
	v_mov_b32_e32 v42, v3
	v_cvt_pk_fp8_f32 v42, v34, 0
	v_cvt_pk_fp8_f32 v38, 0, 0 op_sel:[0,0,1]
	v_cvt_pk_fp8_f32 v36, 0, 0 op_sel:[0,0,1]
	v_mad_i64_i32 v[48:49], s[6:7], v28, s0, v[6:7]
	v_mul_f32_e32 v28, v5, v32
	v_cvt_pk_fp8_f32 v40, 0, 0 op_sel:[0,0,1]
	v_cvt_pk_fp8_f32 v42, 0, 0 op_sel:[0,0,1]
	v_fma_f32 v28, v4, v30, -v28
	v_mul_f32_e32 v30, v5, v30
	v_fmac_f32_e32 v30, v4, v32
	v_add_f32_e32 v28, v59, v28
	v_add_f32_e32 v30, v55, v30
	global_store_byte v[56:57], v38, off sc1
	global_store_byte v[56:57], v40, off offset:64 sc1
	global_store_byte v[48:49], v36, off sc1
	global_store_byte v[48:49], v42, off offset:64 sc1
	v_mul_f32_e32 v32, 0x43000000, v28
	v_mad_i64_i32 v[48:49], s[6:7], v26, s0, v[6:7]
	v_mul_f32_e32 v26, v5, v30
	v_med3_f32 v32, v32, s1, v13
	v_mov_b32_e32 v34, v3
	v_fma_f32 v26, v4, v28, -v26
	v_cvt_pk_fp8_f32 v34, v32, 0
	v_mul_f32_e32 v32, 0x43000000, v30
	v_add_f32_e32 v26, v51, v26
	v_mul_f32_e32 v28, v5, v28
	v_med3_f32 v32, v32, s1, v13
	v_mov_b32_e32 v36, v3
	v_fmac_f32_e32 v28, v4, v30
	v_mul_f32_e32 v30, 0x43000000, v26
	v_cvt_pk_fp8_f32 v36, v32, 0
	v_add_f32_e32 v28, v47, v28
	v_med3_f32 v30, v30, s1, v13
	v_mov_b32_e32 v32, v3
	v_cvt_pk_fp8_f32 v32, v30, 0
	v_mul_f32_e32 v30, 0x43000000, v28
	v_med3_f32 v30, v30, s1, v13
	v_mov_b32_e32 v38, v3
	v_cvt_pk_fp8_f32 v38, v30, 0
	v_mad_i64_i32 v[46:47], s[6:7], v24, s0, v[6:7]
	v_mul_f32_e32 v24, v5, v28
	v_fma_f32 v24, v4, v26, -v24
	v_mul_f32_e32 v26, v5, v26
	v_cvt_pk_fp8_f32 v34, 0, 0 op_sel:[0,0,1]
	v_cvt_pk_fp8_f32 v32, 0, 0 op_sel:[0,0,1]
	v_add_f32_e32 v24, v45, v24
	v_fmac_f32_e32 v26, v4, v28
	v_cvt_pk_fp8_f32 v36, 0, 0 op_sel:[0,0,1]
	v_cvt_pk_fp8_f32 v38, 0, 0 op_sel:[0,0,1]
	v_add_f32_e32 v26, v41, v26
	v_mul_f32_e32 v28, 0x43000000, v24
	v_med3_f32 v28, v28, s1, v13
	v_mov_b32_e32 v30, v3
	v_mad_i64_i32 v[40:41], s[6:7], v22, s0, v[6:7]
	v_mul_f32_e32 v22, v5, v26
	v_cvt_pk_fp8_f32 v30, v28, 0
	v_mul_f32_e32 v28, 0x43000000, v26
	v_fma_f32 v22, v4, v24, -v22
	global_store_byte v[48:49], v34, off sc1
	global_store_byte v[48:49], v36, off offset:64 sc1
	global_store_byte v[46:47], v32, off sc1
	global_store_byte v[46:47], v38, off offset:64 sc1
	v_med3_f32 v28, v28, s1, v13
	v_mov_b32_e32 v32, v3
	v_add_f32_e32 v22, v37, v22
	v_mul_f32_e32 v24, v5, v24
	v_cvt_pk_fp8_f32 v32, v28, 0
	v_fmac_f32_e32 v24, v4, v26
	v_mul_f32_e32 v26, 0x43000000, v22
	v_add_f32_e32 v24, v33, v24
	v_med3_f32 v26, v26, s1, v13
	v_mov_b32_e32 v28, v3
	v_cvt_pk_fp8_f32 v28, v26, 0
	v_mul_f32_e32 v26, 0x43000000, v24
	v_cvt_pk_fp8_f32 v30, 0, 0 op_sel:[0,0,1]
	v_med3_f32 v26, v26, s1, v13
	v_mov_b32_e32 v34, v3
	v_cvt_pk_fp8_f32 v32, 0, 0 op_sel:[0,0,1]
	v_cvt_pk_fp8_f32 v34, v26, 0
	global_store_byte v[40:41], v30, off sc1
	global_store_byte v[40:41], v32, off offset:64 sc1
	v_cvt_pk_fp8_f32 v28, 0, 0 op_sel:[0,0,1]
	v_mad_i64_i32 v[32:33], s[6:7], v20, s0, v[6:7]
	v_mul_f32_e32 v20, v5, v24
	v_cvt_pk_fp8_f32 v34, 0, 0 op_sel:[0,0,1]
	v_fma_f32 v20, v4, v22, -v20
	v_mul_f32_e32 v22, v5, v22
	v_fmac_f32_e32 v22, v4, v24
	v_add_f32_e32 v20, v43, v20
	v_add_f32_e32 v22, v39, v22
	global_store_byte v[32:33], v28, off sc1
	global_store_byte v[32:33], v34, off offset:64 sc1
	v_mul_f32_e32 v24, 0x43000000, v20
	v_mad_i64_i32 v[32:33], s[6:7], v18, s0, v[6:7]
	v_mul_f32_e32 v18, v5, v22
	v_med3_f32 v24, v24, s1, v13
	v_mov_b32_e32 v26, v3
	v_fma_f32 v18, v4, v20, -v18
	v_cvt_pk_fp8_f32 v26, v24, 0
	v_mul_f32_e32 v24, 0x43000000, v22
	v_add_f32_e32 v18, v35, v18
	v_mul_f32_e32 v20, v5, v20
	v_med3_f32 v24, v24, s1, v13
	v_mov_b32_e32 v28, v3
	v_fmac_f32_e32 v20, v4, v22
	v_mul_f32_e32 v22, 0x43000000, v18
	v_cvt_pk_fp8_f32 v28, v24, 0
; __device__ __forceinline__ void phase_carry(Frame& F, int l) {
;     ...
; #pragma unroll
;     for (int step = 0; step < 36; ++step) {
;         int inst; if (step < 4) inst = 256 + b * 4 + (d == 0 ? step : 3 - step); else inst = b * 32 + (d == 0 ? step - 4 : 35 - step);
;         const size_t row = (size_t)g * NINST + inst;
;         a8[row * KS2 + 1024 + d * 128 + p] = (unsigned char)(pk4_fp8(hr * S5_SH, 0.f, 0.f, 0.f) & 0xffu); a8[row * KS2 + 1024 + d * 128 + 64 + p] = (unsigned char)(pk4_fp8(hi * S5_SH, 0.f, 0.f, 0.f) & 0xffu);
;         const float nr = lt.x * hr - lt.y * hi + frv[step]; hi = lt.x * hi + lt.y * hr + fiv[step]; hr = nr; }
	v_add_f32_e32 v20, v31, v20
	v_med3_f32 v22, v22, s1, v13
	v_mov_b32_e32 v24, v3
	v_cvt_pk_fp8_f32 v24, v22, 0
	v_mul_f32_e32 v22, 0x43000000, v20
	v_med3_f32 v22, v22, s1, v13
	v_mov_b32_e32 v34, v3
	v_cvt_pk_fp8_f32 v26, 0, 0 op_sel:[0,0,1]
	v_cvt_pk_fp8_f32 v34, v22, 0
	v_mad_i64_i32 v[30:31], s[6:7], v16, s0, v[6:7]
	v_mul_f32_e32 v16, v5, v20
	v_cvt_pk_fp8_f32 v28, 0, 0 op_sel:[0,0,1]
	v_fma_f32 v16, v4, v18, -v16
	v_mul_f32_e32 v18, v5, v18
	v_fmac_f32_e32 v18, v4, v20
	v_cvt_pk_fp8_f32 v24, 0, 0 op_sel:[0,0,1]
	v_add_f32_e32 v16, v29, v16
	v_add_f32_e32 v18, v27, v18
	global_store_byte v[32:33], v26, off sc1
	global_store_byte v[32:33], v28, off offset:64 sc1
	v_cvt_pk_fp8_f32 v34, 0, 0 op_sel:[0,0,1]
	v_mul_f32_e32 v20, 0x43000000, v16
	v_mad_i64_i32 v[26:27], s[6:7], v14, s0, v[6:7]
	v_mul_f32_e32 v14, v5, v18
	v_med3_f32 v20, v20, s1, v13
	v_mov_b32_e32 v22, v3
	v_fma_f32 v14, v4, v16, -v14
	v_cvt_pk_fp8_f32 v22, v20, 0
	v_mul_f32_e32 v20, 0x43000000, v18
	v_add_f32_e32 v14, v21, v14
	v_mul_f32_e32 v16, v5, v16
	global_store_byte v[30:31], v24, off sc1
	global_store_byte v[30:31], v34, off offset:64 sc1
	v_med3_f32 v20, v20, s1, v13
	v_mov_b32_e32 v24, v3
	v_fmac_f32_e32 v16, v4, v18
	v_mul_f32_e32 v18, 0x43000000, v14
	v_cvt_pk_fp8_f32 v24, v20, 0
	v_add_f32_e32 v16, v19, v16
	v_med3_f32 v18, v18, s1, v13
	v_mov_b32_e32 v20, v3
	v_cvt_pk_fp8_f32 v20, v18, 0
	v_mul_f32_e32 v18, 0x43000000, v16
	v_med3_f32 v18, v18, s1, v13
	v_mov_b32_e32 v21, v3
	v_cvt_pk_fp8_f32 v21, v18, 0
	v_cvt_pk_fp8_f32 v22, 0, 0 op_sel:[0,0,1]
	v_cvt_pk_fp8_f32 v20, 0, 0 op_sel:[0,0,1]
	v_mad_i64_i32 v[18:19], s[6:7], v12, s0, v[6:7]
	v_mul_f32_e32 v12, v5, v16
	v_cvt_pk_fp8_f32 v24, 0, 0 op_sel:[0,0,1]
	v_cvt_pk_fp8_f32 v21, 0, 0 op_sel:[0,0,1]
	v_fma_f32 v12, v4, v14, -v12
	v_mul_f32_e32 v14, v5, v14
	v_fmac_f32_e32 v14, v4, v16
	v_add_f32_e32 v12, v25, v12
	v_add_f32_e32 v14, v23, v14
	global_store_byte v[26:27], v22, off sc1
	global_store_byte v[26:27], v24, off offset:64 sc1
	global_store_byte v[18:19], v20, off sc1
	global_store_byte v[18:19], v21, off offset:64 sc1
	v_mul_f32_e32 v16, 0x43000000, v12
	v_mad_i64_i32 v[18:19], s[6:7], v10, s0, v[6:7]
	v_mul_f32_e32 v10, v5, v14
	v_med3_f32 v16, v16, s1, v13
	v_mov_b32_e32 v20, v3
	v_fma_f32 v10, v4, v12, -v10
	v_cvt_pk_fp8_f32 v20, v16, 0
	v_mul_f32_e32 v16, 0x43000000, v14
	v_add_f32_e32 v10, v17, v10
	v_mul_f32_e32 v12, v5, v12
	v_med3_f32 v16, v16, s1, v13
	v_mov_b32_e32 v21, v3
	v_fmac_f32_e32 v12, v4, v14
	v_mul_f32_e32 v14, 0x43000000, v10
	v_cvt_pk_fp8_f32 v21, v16, 0
	v_add_f32_e32 v12, v15, v12
	v_med3_f32 v14, v14, s1, v13
	v_mov_b32_e32 v16, v3
	v_cvt_pk_fp8_f32 v16, v14, 0
	v_mul_f32_e32 v14, 0x43000000, v12
	v_med3_f32 v14, v14, s1, v13
	v_mov_b32_e32 v17, v3
	v_cvt_pk_fp8_f32 v17, v14, 0
	v_mad_i64_i32 v[14:15], s[6:7], v8, s0, v[6:7]
	v_mul_f32_e32 v8, v5, v12
	v_fma_f32 v8, v4, v10, -v8
	v_mul_f32_e32 v5, v5, v10
	v_add_f32_e32 v8, v11, v8
	v_fmac_f32_e32 v5, v4, v12
	v_add_f32_e32 v4, v9, v5
	v_mul_f32_e32 v8, 0x43000000, v8
	v_med3_f32 v8, v8, s1, v13
	v_mov_b32_e32 v9, v3
	v_mul_f32_e32 v4, 0x43000000, v4
	v_cvt_pk_fp8_f32 v9, v8, 0
	v_med3_f32 v4, v4, s1, v13
	v_cvt_pk_fp8_f32 v3, v4, 0
	v_cvt_pk_fp8_f32 v20, 0, 0 op_sel:[0,0,1]
	v_cvt_pk_fp8_f32 v16, 0, 0 op_sel:[0,0,1]
	v_cndmask_b32_e64 v5, 0, 31, vcc
	v_cvt_pk_fp8_f32 v9, 0, 0 op_sel:[0,0,1]
	v_cvt_pk_fp8_f32 v21, 0, 0 op_sel:[0,0,1]
	v_cvt_pk_fp8_f32 v17, 0, 0 op_sel:[0,0,1]
	v_or_b32_e32 v1, v1, v5
	v_cvt_pk_fp8_f32 v3, 0, 0 op_sel:[0,0,1]
	v_add_u32_e32 v1, v1, v2
	v_mad_i64_i32 v[4:5], s[0:1], v1, s0, v[6:7]
	global_store_byte v[18:19], v20, off sc1
	global_store_byte v[18:19], v21, off offset:64 sc1
	global_store_byte v[14:15], v16, off sc1
	global_store_byte v[14:15], v17, off offset:64 sc1
	global_store_byte v[4:5], v9, off sc1
	global_store_byte v[4:5], v3, off offset:64 sc1
.Lfd1_1501:
	s_or_b64 exec, exec, s[4:5]
	s_waitcnt vmcnt(0) lgkmcnt(0)
	v_readlane_b32 s0, v254, 0
	v_readlane_b32 s1, v254, 1
	v_readlane_b32 s2, v254, 2
	v_readlane_b32 s3, v254, 3
	v_readlane_b32 s4, v254, 4
	v_readlane_b32 s5, v254, 5
	v_readlane_b32 s6, v254, 6
	v_readlane_b32 s7, v254, 7
	v_readlane_b32 s33, v254, 8
	v_readlane_b32 s40, v254, 9
	s_barrier
	v_cmp_eq_u32_e64 s[98:99], 0, v0
	s_and_saveexec_b64 s[100:101], s[98:99]
	s_cbranch_execz .Lfs1_pw
	v_mov_b32_e32 v2, s33
	v_mov_b32_e32 v3, s40
	v_mov_b32_e32 v4, 1
	flat_atomic_add v[2:3], v4 offset:3848
	s_waitcnt vmcnt(0) lgkmcnt(0)

; #define LAS __attribute__((address_space(3)))
; __device__ __forceinline__ unsigned xb_add(unsigned* p, unsigned v) { return __hip_atomic_fetch_add(p, v, __ATOMIC_RELAXED, __HIP_MEMORY_SCOPE_AGENT); }
; __device__ __forceinline__ unsigned xb_xcc_id() { return (unsigned)__builtin_amdgcn_s_getreg((3 << 11) | 20) & 0xFu; }
; __device__ __forceinline__ void xcd_barrier(const XcdBarrier& b) {
;     asm volatile("s_waitcnt vmcnt(0)" ::: "memory");
;     __syncthreads();
;     if (threadIdx.x == 0) {
;         unsigned* bar = b.bar;
;         __builtin_amdgcn_s_waitcnt(0);
;         unsigned nloc = b.st[0], nx = b.st[1];
;         if (nloc == 0u) { xcd_barrier_complete(bar, b.x, nloc, nx); b.st[0] = nloc; b.st[1] = nx; }
;         const unsigned old = xb_add(&bar[XB_XSUB(b.x)], 1u);
; __device__ __forceinline__ void grid_seam(Frame& F) {
;     XcdBarrier b; b.bar = (unsigned*)(F.ws + WS_CTL) + CW_BAR; b.x = xb_xcc_id(); b.st = (volatile LAS unsigned*)(F.lds + MISC_OFF) + 8;
;     xcd_barrier(b);
; }
.Lfd1_done:
	s_branch .Lfs1_end
	s_getreg_b32 s0, hwreg(HW_REG_XCC_ID, 0, 4)
	s_waitcnt vmcnt(0)
	s_waitcnt vmcnt(0)
	s_barrier
	s_mov_b64 s[2:3], exec
	v_readlane_b32 s4, v249, 3
	v_readlane_b32 s5, v249, 4
	s_and_b64 s[4:5], s[2:3], s[4:5]
	s_xor_b64 s[2:3], s[4:5], s[2:3]
	s_mov_b64 exec, s[4:5]
	s_cbranch_execz .LBB0_1497
	s_add_i32 s1, 0, 0x20160
	v_mov_b32_e32 v1, s1
	s_waitcnt vmcnt(0) expcnt(0) lgkmcnt(0)
	ds_read_b32 v4, v1
	s_add_i32 s1, 0, 0x20164
	v_mov_b32_e32 v1, s1
	ds_read_b32 v2, v1
	s_and_b32 s43, s0, 15
	s_waitcnt lgkmcnt(1)
	v_cmp_ne_u32_e32 vcc, 0, v4
	s_cbranch_vccnz .LBB0_1467
	v_readlane_b32 s6, v249, 0
	v_readlane_b32 s7, v249, 1
	s_load_dword s4, s[6:7], 0x14
	s_load_dwordx2 s[0:1], s[6:7], 0x4
	s_mov_b32 s23, 1
	s_waitcnt lgkmcnt(0)
	s_lshr_b32 s6, s4, 16
	s_and_b32 s4, s4, 0xffff
	s_cmp_lg_u32 s4, 0
	s_cselect_b64 s[4:5], -1, 0
	s_cmp_lg_u64 s[4:5], 0
	s_addc_u32 s0, s0, 0
	s_cmp_lg_u32 s6, 0
	s_cselect_b64 s[4:5], -1, 0
	s_cmp_lg_u64 s[4:5], 0
	s_mul_i32 s22, s0, s54
	s_addc_u32 s0, s1, 0
	s_add_u32 s4, s33, 0x4200
	s_addc_u32 s5, s40, 0
	s_add_u32 s6, s33, 0x4400
	s_addc_u32 s7, s40, 0
	s_add_u32 s8, s33, 0x4500
	s_addc_u32 s9, s40, 0
	s_add_u32 s10, s33, 0x4600
	s_addc_u32 s11, s40, 0
	s_add_u32 s12, s33, 0x4700
	s_addc_u32 s13, s40, 0
	s_add_u32 s14, s33, 0x4800
	s_addc_u32 s15, s40, 0
	s_add_u32 s16, s33, 0x4900
	s_addc_u32 s17, s40, 0
	s_add_u32 s18, s33, 0x4a00
	s_addc_u32 s19, s40, 0
	s_add_u32 s20, s33, 0x4b00
	s_addc_u32 s21, s40, 0
	s_add_u32 s24, s33, 0x4c00
	s_addc_u32 s25, s40, 0
	s_add_u32 s26, s33, 0x4d00
	s_addc_u32 s27, s40, 0
	s_add_u32 s28, s33, 0x4e00
	s_addc_u32 s29, s40, 0
	s_add_u32 s30, s33, 0x4f00
	s_addc_u32 s31, s40, 0
	s_add_u32 s34, s33, 0x5000
	s_addc_u32 s35, s40, 0
	s_add_u32 s36, s33, 0x5100
	s_addc_u32 s37, s40, 0
	s_add_u32 s44, s33, 0x5200
	s_addc_u32 s45, s40, 0
	s_add_u32 s46, s33, 0x5300
	s_addc_u32 s47, s40, 0
	s_mul_i32 s22, s22, s0
	s_mov_b64 s[0:1], 0
	v_mov_b64_e32 v[2:3], s[6:7]
	v_mov_b64_e32 v[4:5], s[8:9]
	v_mov_b64_e32 v[6:7], s[10:11]
	v_mov_b64_e32 v[8:9], s[12:13]
	v_mov_b64_e32 v[10:11], s[14:15]
	v_mov_b64_e32 v[12:13], s[16:17]
	v_mov_b64_e32 v[14:15], s[18:19]
	v_mov_b64_e32 v[16:17], s[20:21]
	v_mov_b64_e32 v[18:19], s[24:25]
	v_mov_b64_e32 v[20:21], s[26:27]
	v_mov_b64_e32 v[22:23], s[28:29]
	v_mov_b64_e32 v[24:25], s[30:31]
	v_mov_b64_e32 v[26:27], s[34:35]
	v_mov_b64_e32 v[28:29], s[36:37]
	v_mov_b64_e32 v[30:31], s[44:45]
	v_mov_b64_e32 v[32:33], s[46:47]
	s_branch .LBB0_1457

; __device__ __forceinline__ void launder(Frame& F) { F.ws = opaque_ptr(F.ws); F.out = opaque_ptr(F.out);
;     int t = F.tid; asm volatile("" : "+v"(t)); F.tid = t; F.lane = t & 63; F.wave = __builtin_amdgcn_readfirstlane(t >> 6);
;     int g = gridDim.x, bx = blockIdx.x; asm volatile("" : "+v"(g), "+v"(bx)); g = __builtin_amdgcn_readfirstlane(g); bx = __builtin_amdgcn_readfirstlane(bx);
;     F.G = g; F.vcu = (g % 8 == 0) ? (bx % 8) * (g / 8) + bx / 8 : bx; }
.Lfs1_end:
	v_mov_b32_e32 v1, s33
	v_mov_b32_e32 v2, s40
	s_waitcnt lgkmcnt(0)
	s_barrier
	s_nop 0
	v_readfirstlane_b32 s2, v1
	v_readfirstlane_b32 s3, v2
	v_mov_b32_e32 v1, s41
	v_mov_b32_e32 v2, s42
	s_nop 0
	v_readfirstlane_b32 s33, v1
	v_readfirstlane_b32 s40, v2
	s_branch .Lfd1_end
	v_mov_b32_e32 v1, s54
	v_mov_b32_e32 v2, s95
	s_nop 0
	v_readfirstlane_b32 s1, v1
	s_and_b32 s0, s1, 7
	s_cmp_eq_u32 s0, 0
	v_readfirstlane_b32 s0, v2
	s_cbranch_scc0 .LBB0_1499
	s_ashr_i32 s4, s0, 31
	s_lshr_b32 s4, s4, 29
	s_add_i32 s4, s0, s4
	s_ashr_i32 s5, s4, 3
	s_and_b32 s4, s4, -8
	s_ashr_i32 s1, s1, 3
	s_sub_i32 s0, s0, s4
	s_mul_i32 s0, s0, s1
	s_add_i32 s0, s0, s5

; __device__ __forceinline__ void wait_ctx_rows(Frame& F) {
;     if (F.wave == 0) { unsigned* cnt = (unsigned*)(F.ws + WS_CTL) + CW_CTXROWS; unsigned sp = 0;
;         while ((unsigned)__builtin_amdgcn_readfirstlane((int)__hip_atomic_load(cnt, __ATOMIC_RELAXED, __HIP_MEMORY_SCOPE_AGENT)) < (unsigned)MC) { __builtin_amdgcn_s_sleep(2); if (++sp > (1u << 22)) break; }
;         __builtin_amdgcn_fence(__ATOMIC_ACQUIRE, "agent");
;         asm volatile("s_waitcnt vmcnt(0)" ::: "memory"); }
;     __syncthreads();
.Lfs1_poll:
	flat_load_dword v4, v[2:3] offset:3848 sc1
	s_waitcnt vmcnt(0) lgkmcnt(0)
	v_readfirstlane_b32 s99, v4
	s_add_u32 s98, s98, 1
	s_cmp_ge_u32 s99, 128
	s_cbranch_scc1 .Lfs1_go
	s_sleep 2
	s_cmp_lt_u32 s98, 0x4000
	s_cbranch_scc1 .Lfs1_poll

; __device__ __forceinline__ void launder(Frame& F) { F.ws = opaque_ptr(F.ws); F.out = opaque_ptr(F.out);
;     int t = F.tid; asm volatile("" : "+v"(t)); F.tid = t; F.lane = t & 63; F.wave = __builtin_amdgcn_readfirstlane(t >> 6);
;     int g = gridDim.x, bx = blockIdx.x; asm volatile("" : "+v"(g), "+v"(bx)); g = __builtin_amdgcn_readfirstlane(g); bx = __builtin_amdgcn_readfirstlane(bx);
;     F.G = g; F.vcu = (g % 8 == 0) ? (bx % 8) * (g / 8) + bx / 8 : bx; }
.Lfs1_w:
	s_or_b64 exec, exec, s[100:101]
	v_mov_b32_e32 v1, s2
	v_mov_b32_e32 v2, s3
	s_waitcnt lgkmcnt(0)
	s_barrier
	s_nop 0
	v_readfirstlane_b32 s42, v1
	v_readfirstlane_b32 s43, v2
	v_mov_b32_e32 v1, s33
	v_mov_b32_e32 v2, s40
	s_nop 0
	v_readfirstlane_b32 s55, v1
	v_readfirstlane_b32 s56, v2
	v_mov_b32_e32 v1, s54
	v_mov_b32_e32 v2, s95
	v_readfirstlane_b32 s33, v0
	v_readfirstlane_b32 s57, v1
	s_and_b32 s0, s57, 7
	s_cmp_eq_u32 s0, 0
	v_readfirstlane_b32 s58, v2
	s_cbranch_scc0 .LBB0_1548
	s_ashr_i32 s1, s58, 31
	s_lshr_b32 s1, s1, 29
	s_add_i32 s1, s58, s1
	s_ashr_i32 s2, s1, 3
	s_and_b32 s1, s1, -8
	s_ashr_i32 s0, s57, 3
	s_sub_i32 s1, s58, s1
	s_mul_i32 s0, s1, s0
	s_add_i32 s58, s0, s2
